# exp_v token loop regenerated (fp4 convert issued 4 slots ahead of its packed fma, register reduce-scatter, hoisted LDS index/coef reads); grid barriers 2-13 without the top word (last workgroup of eac
# speedup vs baseline: 1.0649x; 1.0649x over previous
.LBB0_2:
	s_or_b64 exec, exec, s[6:7]
	s_mov_b64 s[6:7], s[0:1]
	s_waitcnt lgkmcnt(0)
	s_barrier
	s_load_dwordx2 s[44:45], s[6:7], 0x220
	s_getreg_b32 s3, hwreg(HW_REG_XCC_ID, 0, 4)
	s_and_b32 s33, s3, 15
	s_and_saveexec_b64 s[6:7], s[4:5]
	s_cbranch_execz .LBB0_5
	s_mov_b64 s[8:9], exec
	v_mbcnt_lo_u32_b32 v1, s8, 0
	v_mbcnt_hi_u32_b32 v1, s9, v1
	v_cmp_eq_u32_e32 vcc, 0, v1
	s_and_b64 s[10:11], exec, vcc
	s_mov_b64 exec, s[10:11]
	s_cbranch_execz .LBB0_5
	s_lshl_b32 s3, s33, 8
	s_bcnt1_i32_b64 s8, s[8:9]
	v_mov_b32_e32 v1, s3
	v_mov_b32_e32 v2, s8
	s_waitcnt lgkmcnt(0)
	global_atomic_add v1, v2, s[44:45] offset:1024
	s_mov_b32 s98, 0

.LBB0_115:
	s_waitcnt vmcnt(0)
	s_barrier
	s_and_saveexec_b64 s[6:7], s[4:5]
	s_cbranch_execz .LBB0_167
	s_waitcnt vmcnt(0) lgkmcnt(0)
	s_add_u32 s98, s98, 1
	v_mov_b32_e32 v253, 0x12810
	ds_read_b32 v254, v253
	ds_read_b32 v253, v253 offset:4
	s_lshl_b32 s101, s33, 8
	s_add_u32 s99, s101, 5120
	s_waitcnt lgkmcnt(0)
	v_readfirstlane_b32 s100, v254
	v_mov_b32_e32 v254, s99
	v_readfirstlane_b32 s99, v253
	s_nop 0
	v_mov_b32_e32 v253, v254
	v_mov_b32_e32 v254, 1
	global_atomic_add v254, v253, v254, s[44:45] offset:64 sc0
	s_mul_i32 s100, s100, s98
	s_mul_i32 s99, s99, s98
	s_waitcnt vmcnt(0)
	v_add_u32_e32 v254, 1, v254
	v_cmp_ne_u32_e32 vcc, s100, v254
	s_cbranch_vccnz .Lgb_wait_2
	buffer_wbl2 sc1
	s_waitcnt vmcnt(0)
	v_mov_b32_e32 v254, 1
	v_mov_b32_e32 v253, 9216
	global_atomic_add v253, v254, s[44:45] offset:64
	global_atomic_add v253, v254, s[44:45] offset:320
	global_atomic_add v253, v254, s[44:45] offset:576
	global_atomic_add v253, v254, s[44:45] offset:832
	global_atomic_add v253, v254, s[44:45] offset:1088
	global_atomic_add v253, v254, s[44:45] offset:1344
	global_atomic_add v253, v254, s[44:45] offset:1600
	global_atomic_add v253, v254, s[44:45] offset:1856
	v_mov_b32_e32 v253, 11264
	global_atomic_add v253, v254, s[44:45] offset:64
	global_atomic_add v253, v254, s[44:45] offset:320
	global_atomic_add v253, v254, s[44:45] offset:576
	global_atomic_add v253, v254, s[44:45] offset:832
	global_atomic_add v253, v254, s[44:45] offset:1088
	global_atomic_add v253, v254, s[44:45] offset:1344
	global_atomic_add v253, v254, s[44:45] offset:1600
	global_atomic_add v253, v254, s[44:45] offset:1856
.Lgb_wait_2:
	s_add_u32 s100, s101, 9216
	v_mov_b32_e32 v253, s100
	s_mov_b32 s100, 0
.Lgb_w_2:
	global_load_dword v254, v253, s[44:45] offset:64 sc1
	s_waitcnt vmcnt(0)
	v_cmp_le_u32_e32 vcc, s99, v254
	s_cbranch_vccnz .Lgb_wd_2
	s_sleep 1
	s_add_u32 s100, s100, 1
	s_cmp_lt_u32 s100, 0x1000
	s_cbranch_scc1 .Lgb_w_2
.Lgb_wd_2:
	buffer_inv sc1
	s_waitcnt vmcnt(0)

.LBB0_179:
	s_or_b64 exec, exec, s[10:11]
	s_waitcnt vmcnt(0)
	s_barrier
	s_and_saveexec_b64 s[6:7], s[4:5]
	s_cbranch_execz .LBB0_231
	s_waitcnt vmcnt(0) lgkmcnt(0)
	s_add_u32 s98, s98, 1
	v_mov_b32_e32 v253, 0x12810
	ds_read_b32 v254, v253
	ds_read_b32 v253, v253 offset:4
	s_lshl_b32 s101, s33, 8
	s_add_u32 s99, s101, 5120
	s_waitcnt lgkmcnt(0)
	v_readfirstlane_b32 s100, v254
	v_mov_b32_e32 v254, s99
	v_readfirstlane_b32 s99, v253
	s_nop 0
	v_mov_b32_e32 v253, v254
	v_mov_b32_e32 v254, 1
	global_atomic_add v254, v253, v254, s[44:45] offset:64 sc0
	s_mul_i32 s100, s100, s98
	s_mul_i32 s99, s99, s98
	s_waitcnt vmcnt(0)
	v_add_u32_e32 v254, 1, v254
	v_cmp_ne_u32_e32 vcc, s100, v254
	s_cbranch_vccnz .Lgb_wait_3
	buffer_wbl2 sc1
	s_waitcnt vmcnt(0)
	v_mov_b32_e32 v254, 1
	v_mov_b32_e32 v253, 9216
	global_atomic_add v253, v254, s[44:45] offset:64
	global_atomic_add v253, v254, s[44:45] offset:320
	global_atomic_add v253, v254, s[44:45] offset:576
	global_atomic_add v253, v254, s[44:45] offset:832
	global_atomic_add v253, v254, s[44:45] offset:1088
	global_atomic_add v253, v254, s[44:45] offset:1344
	global_atomic_add v253, v254, s[44:45] offset:1600
	global_atomic_add v253, v254, s[44:45] offset:1856
	v_mov_b32_e32 v253, 11264
	global_atomic_add v253, v254, s[44:45] offset:64
	global_atomic_add v253, v254, s[44:45] offset:320
	global_atomic_add v253, v254, s[44:45] offset:576
	global_atomic_add v253, v254, s[44:45] offset:832
	global_atomic_add v253, v254, s[44:45] offset:1088
	global_atomic_add v253, v254, s[44:45] offset:1344
	global_atomic_add v253, v254, s[44:45] offset:1600
	global_atomic_add v253, v254, s[44:45] offset:1856

.LBB0_572:
	s_waitcnt vmcnt(0)
	s_waitcnt lgkmcnt(0)
	s_barrier
	s_and_saveexec_b64 s[6:7], s[4:5]
	s_cbranch_execz .LBB0_624
	s_waitcnt vmcnt(0) lgkmcnt(0)
	s_add_u32 s98, s98, 1
	v_mov_b32_e32 v253, 0x12810
	ds_read_b32 v254, v253
	ds_read_b32 v253, v253 offset:4
	s_lshl_b32 s101, s33, 8
	s_add_u32 s99, s101, 5120
	s_waitcnt lgkmcnt(0)
	v_readfirstlane_b32 s100, v254
	v_mov_b32_e32 v254, s99
	v_readfirstlane_b32 s99, v253
	s_nop 0
	v_mov_b32_e32 v253, v254
	v_mov_b32_e32 v254, 1
	global_atomic_add v254, v253, v254, s[44:45] offset:64 sc0
	s_mul_i32 s100, s100, s98
	s_mul_i32 s99, s99, s98
	s_waitcnt vmcnt(0)
	v_add_u32_e32 v254, 1, v254
	v_cmp_ne_u32_e32 vcc, s100, v254
	s_cbranch_vccnz .Lgb_wait_4
	buffer_wbl2 sc1
	s_waitcnt vmcnt(0)
	v_mov_b32_e32 v254, 1
	v_mov_b32_e32 v253, 9216
	global_atomic_add v253, v254, s[44:45] offset:64
	global_atomic_add v253, v254, s[44:45] offset:320
	global_atomic_add v253, v254, s[44:45] offset:576
	global_atomic_add v253, v254, s[44:45] offset:832
	global_atomic_add v253, v254, s[44:45] offset:1088
	global_atomic_add v253, v254, s[44:45] offset:1344
	global_atomic_add v253, v254, s[44:45] offset:1600
	global_atomic_add v253, v254, s[44:45] offset:1856
	v_mov_b32_e32 v253, 11264
	global_atomic_add v253, v254, s[44:45] offset:64
	global_atomic_add v253, v254, s[44:45] offset:320
	global_atomic_add v253, v254, s[44:45] offset:576
	global_atomic_add v253, v254, s[44:45] offset:832
	global_atomic_add v253, v254, s[44:45] offset:1088
	global_atomic_add v253, v254, s[44:45] offset:1344
	global_atomic_add v253, v254, s[44:45] offset:1600
	global_atomic_add v253, v254, s[44:45] offset:1856

.LBB0_677:
	s_or_b64 exec, exec, s[12:13]
	s_waitcnt vmcnt(0)
	s_waitcnt lgkmcnt(0)
	s_barrier
	s_and_saveexec_b64 s[6:7], s[4:5]
	s_cbranch_execz .LBB0_729
	s_waitcnt vmcnt(0) lgkmcnt(0)
	s_add_u32 s98, s98, 1
	v_mov_b32_e32 v253, 0x12810
	ds_read_b32 v254, v253
	ds_read_b32 v253, v253 offset:4
	s_lshl_b32 s101, s33, 8
	s_add_u32 s99, s101, 5120
	s_waitcnt lgkmcnt(0)
	v_readfirstlane_b32 s100, v254
	v_mov_b32_e32 v254, s99
	v_readfirstlane_b32 s99, v253
	s_nop 0
	v_mov_b32_e32 v253, v254
	v_mov_b32_e32 v254, 1
	global_atomic_add v254, v253, v254, s[44:45] offset:64 sc0
	s_mul_i32 s100, s100, s98
	s_mul_i32 s99, s99, s98
	s_waitcnt vmcnt(0)
	v_add_u32_e32 v254, 1, v254
	v_cmp_ne_u32_e32 vcc, s100, v254
	s_cbranch_vccnz .Lgb_wait_5
	buffer_wbl2 sc1
	s_waitcnt vmcnt(0)
	v_mov_b32_e32 v254, 1
	v_mov_b32_e32 v253, 9216
	global_atomic_add v253, v254, s[44:45] offset:64
	global_atomic_add v253, v254, s[44:45] offset:320
	global_atomic_add v253, v254, s[44:45] offset:576
	global_atomic_add v253, v254, s[44:45] offset:832
	global_atomic_add v253, v254, s[44:45] offset:1088
	global_atomic_add v253, v254, s[44:45] offset:1344
	global_atomic_add v253, v254, s[44:45] offset:1600
	global_atomic_add v253, v254, s[44:45] offset:1856
	v_mov_b32_e32 v253, 11264
	global_atomic_add v253, v254, s[44:45] offset:64
	global_atomic_add v253, v254, s[44:45] offset:320
	global_atomic_add v253, v254, s[44:45] offset:576
	global_atomic_add v253, v254, s[44:45] offset:832
	global_atomic_add v253, v254, s[44:45] offset:1088
	global_atomic_add v253, v254, s[44:45] offset:1344
	global_atomic_add v253, v254, s[44:45] offset:1600
	global_atomic_add v253, v254, s[44:45] offset:1856

.LBB0_1015:
	s_or_b64 exec, exec, s[12:13]
	s_waitcnt vmcnt(0)
	s_barrier
	s_and_saveexec_b64 s[12:13], s[4:5]
	s_cbranch_execz .LBB0_1067
	s_waitcnt vmcnt(0) lgkmcnt(0)
	s_add_u32 s98, s98, 1
	v_mov_b32_e32 v253, 0x12810
	ds_read_b32 v254, v253
	ds_read_b32 v253, v253 offset:4
	s_lshl_b32 s101, s33, 8
	s_add_u32 s99, s101, 5120
	s_waitcnt lgkmcnt(0)
	v_readfirstlane_b32 s100, v254
	v_mov_b32_e32 v254, s99
	v_readfirstlane_b32 s99, v253
	s_nop 0
	v_mov_b32_e32 v253, v254
	v_mov_b32_e32 v254, 1
	global_atomic_add v254, v253, v254, s[44:45] offset:64 sc0
	s_mul_i32 s100, s100, s98
	s_mul_i32 s99, s99, s98
	s_waitcnt vmcnt(0)
	v_add_u32_e32 v254, 1, v254
	v_cmp_ne_u32_e32 vcc, s100, v254
	s_cbranch_vccnz .Lgb_wait_7
	buffer_wbl2 sc1
	s_waitcnt vmcnt(0)
	v_mov_b32_e32 v254, 1
	v_mov_b32_e32 v253, 9216
	global_atomic_add v253, v254, s[44:45] offset:64
	global_atomic_add v253, v254, s[44:45] offset:320
	global_atomic_add v253, v254, s[44:45] offset:576
	global_atomic_add v253, v254, s[44:45] offset:832
	global_atomic_add v253, v254, s[44:45] offset:1088
	global_atomic_add v253, v254, s[44:45] offset:1344
	global_atomic_add v253, v254, s[44:45] offset:1600
	global_atomic_add v253, v254, s[44:45] offset:1856
	v_mov_b32_e32 v253, 11264
	global_atomic_add v253, v254, s[44:45] offset:64
	global_atomic_add v253, v254, s[44:45] offset:320
	global_atomic_add v253, v254, s[44:45] offset:576
	global_atomic_add v253, v254, s[44:45] offset:832
	global_atomic_add v253, v254, s[44:45] offset:1088
	global_atomic_add v253, v254, s[44:45] offset:1344
	global_atomic_add v253, v254, s[44:45] offset:1600
	global_atomic_add v253, v254, s[44:45] offset:1856

.LBB0_1072:
	s_waitcnt vmcnt(0)
	s_waitcnt vmcnt(63) expcnt(7) lgkmcnt(15)
	s_barrier
	s_and_saveexec_b64 s[12:13], s[4:5]
	s_cbranch_execz .LBB0_1124
	s_waitcnt vmcnt(0) lgkmcnt(0)
	s_add_u32 s98, s98, 1
	v_mov_b32_e32 v253, 0x12810
	ds_read_b32 v254, v253
	ds_read_b32 v253, v253 offset:4
	s_lshl_b32 s101, s33, 8
	s_add_u32 s99, s101, 5120
	s_waitcnt lgkmcnt(0)
	v_readfirstlane_b32 s100, v254
	v_mov_b32_e32 v254, s99
	v_readfirstlane_b32 s99, v253
	s_nop 0
	v_mov_b32_e32 v253, v254
	v_mov_b32_e32 v254, 1
	global_atomic_add v254, v253, v254, s[44:45] offset:64 sc0
	s_mul_i32 s100, s100, s98
	s_mul_i32 s99, s99, s98
	s_waitcnt vmcnt(0)
	v_add_u32_e32 v254, 1, v254
	v_cmp_ne_u32_e32 vcc, s100, v254
	s_cbranch_vccnz .Lgb_wait_8
	buffer_wbl2 sc1
	s_waitcnt vmcnt(0)
	v_mov_b32_e32 v254, 1
	v_mov_b32_e32 v253, 9216
	global_atomic_add v253, v254, s[44:45] offset:64
	global_atomic_add v253, v254, s[44:45] offset:320
	global_atomic_add v253, v254, s[44:45] offset:576
	global_atomic_add v253, v254, s[44:45] offset:832
	global_atomic_add v253, v254, s[44:45] offset:1088
	global_atomic_add v253, v254, s[44:45] offset:1344
	global_atomic_add v253, v254, s[44:45] offset:1600
	global_atomic_add v253, v254, s[44:45] offset:1856
	v_mov_b32_e32 v253, 11264
	global_atomic_add v253, v254, s[44:45] offset:64
	global_atomic_add v253, v254, s[44:45] offset:320
	global_atomic_add v253, v254, s[44:45] offset:576
	global_atomic_add v253, v254, s[44:45] offset:832
	global_atomic_add v253, v254, s[44:45] offset:1088
	global_atomic_add v253, v254, s[44:45] offset:1344
	global_atomic_add v253, v254, s[44:45] offset:1600
	global_atomic_add v253, v254, s[44:45] offset:1856

.LBB0_1131:
	s_or_b64 exec, exec, s[20:21]
	s_waitcnt vmcnt(0)
	s_barrier
	s_and_saveexec_b64 s[8:9], s[4:5]
	s_cbranch_execz .LBB0_1183
	s_waitcnt vmcnt(0) lgkmcnt(0)
	s_add_u32 s98, s98, 1
	v_mov_b32_e32 v253, 0x12810
	ds_read_b32 v254, v253
	ds_read_b32 v253, v253 offset:4
	s_lshl_b32 s101, s33, 8
	s_add_u32 s99, s101, 5120
	s_waitcnt lgkmcnt(0)
	v_readfirstlane_b32 s100, v254
	v_mov_b32_e32 v254, s99
	v_readfirstlane_b32 s99, v253
	s_nop 0
	v_mov_b32_e32 v253, v254
	v_mov_b32_e32 v254, 1
	global_atomic_add v254, v253, v254, s[44:45] offset:64 sc0
	s_mul_i32 s100, s100, s98
	s_mul_i32 s99, s99, s98
	s_waitcnt vmcnt(0)
	v_add_u32_e32 v254, 1, v254
	v_cmp_ne_u32_e32 vcc, s100, v254
	s_cbranch_vccnz .Lgb_wait_9
	buffer_wbl2 sc1
	s_waitcnt vmcnt(0)
	v_mov_b32_e32 v254, 1
	v_mov_b32_e32 v253, 9216
	global_atomic_add v253, v254, s[44:45] offset:64
	global_atomic_add v253, v254, s[44:45] offset:320
	global_atomic_add v253, v254, s[44:45] offset:576
	global_atomic_add v253, v254, s[44:45] offset:832
	global_atomic_add v253, v254, s[44:45] offset:1088
	global_atomic_add v253, v254, s[44:45] offset:1344
	global_atomic_add v253, v254, s[44:45] offset:1600
	global_atomic_add v253, v254, s[44:45] offset:1856
	v_mov_b32_e32 v253, 11264
	global_atomic_add v253, v254, s[44:45] offset:64
	global_atomic_add v253, v254, s[44:45] offset:320
	global_atomic_add v253, v254, s[44:45] offset:576
	global_atomic_add v253, v254, s[44:45] offset:832
	global_atomic_add v253, v254, s[44:45] offset:1088
	global_atomic_add v253, v254, s[44:45] offset:1344
	global_atomic_add v253, v254, s[44:45] offset:1600
	global_atomic_add v253, v254, s[44:45] offset:1856

.LBB0_1196:
	s_waitcnt vmcnt(0)
	s_barrier
	s_and_saveexec_b64 s[2:3], s[4:5]
	s_cbranch_execz .LBB0_1248
	s_waitcnt vmcnt(0) lgkmcnt(0)
	s_add_u32 s98, s98, 1
	v_mov_b32_e32 v253, 0x12810
	ds_read_b32 v254, v253
	ds_read_b32 v253, v253 offset:4
	s_lshl_b32 s101, s33, 8
	s_add_u32 s99, s101, 5120
	s_waitcnt lgkmcnt(0)
	v_readfirstlane_b32 s100, v254
	v_mov_b32_e32 v254, s99
	v_readfirstlane_b32 s99, v253
	s_nop 0
	v_mov_b32_e32 v253, v254
	v_mov_b32_e32 v254, 1
	global_atomic_add v254, v253, v254, s[44:45] offset:64 sc0
	s_mul_i32 s100, s100, s98
	s_mul_i32 s99, s99, s98
	s_waitcnt vmcnt(0)
	v_add_u32_e32 v254, 1, v254
	v_cmp_ne_u32_e32 vcc, s100, v254
	s_cbranch_vccnz .Lgb_wait_10
	buffer_wbl2 sc1
	s_waitcnt vmcnt(0)
	v_mov_b32_e32 v254, 1
	v_mov_b32_e32 v253, 9216
	global_atomic_add v253, v254, s[44:45] offset:64
	global_atomic_add v253, v254, s[44:45] offset:320
	global_atomic_add v253, v254, s[44:45] offset:576
	global_atomic_add v253, v254, s[44:45] offset:832
	global_atomic_add v253, v254, s[44:45] offset:1088
	global_atomic_add v253, v254, s[44:45] offset:1344
	global_atomic_add v253, v254, s[44:45] offset:1600
	global_atomic_add v253, v254, s[44:45] offset:1856
	v_mov_b32_e32 v253, 11264
	global_atomic_add v253, v254, s[44:45] offset:64
	global_atomic_add v253, v254, s[44:45] offset:320
	global_atomic_add v253, v254, s[44:45] offset:576
	global_atomic_add v253, v254, s[44:45] offset:832
	global_atomic_add v253, v254, s[44:45] offset:1088
	global_atomic_add v253, v254, s[44:45] offset:1344
	global_atomic_add v253, v254, s[44:45] offset:1600
	global_atomic_add v253, v254, s[44:45] offset:1856

.LBB0_1254:
	v_mov_b32_e32 v4, v48
	v_add_u32_e32 v2, s35, v4
	v_and_b32_e32 v3, 7, v2
	v_lshlrev_b32_e32 v2, 8, v3
	global_atomic_add v5, v2, v47, s[44:45] offset:1088 sc0
	s_or_b64 s[50:51], s[50:51], exec
	s_or_b64 s[52:53], s[52:53], exec
	s_waitcnt vmcnt(0)
	v_cmp_lt_i32_e32 vcc, s46, v5
	s_and_saveexec_b64 s[54:55], vcc
	s_cbranch_execz .LBB0_1253
	v_mov_b32_e32 v253, 0x12810
	ds_read_b32 v254, v253 offset:4
	ds_read_b32 v253, v253
	s_waitcnt lgkmcnt(0)
	v_lshlrev_b32_e32 v253, 3, v253
	v_xor_b32_e32 v253, s34, v253
	v_xor_b32_e32 v254, 8, v254
	v_or_b32_e32 v253, v253, v254
	v_cmp_eq_u32_e32 vcc, 0, v253
	v_mov_b32_e32 v254, 7
	s_nop 1
	v_cndmask_b32_e32 v253, v4, v254, vcc
	v_cmp_lt_u32_e32 vcc, 6, v253
	s_andn2_b64 s[52:53], s[52:53], exec
	s_and_b64 s[56:57], vcc, exec
	v_add_u32_e32 v48, 1, v4
	s_andn2_b64 s[50:51], s[50:51], exec
	s_or_b64 s[52:53], s[52:53], s[56:57]
	s_branch .LBB0_1253

.LBB0_1327:
	s_or_b64 exec, exec, s[2:3]
	s_waitcnt vmcnt(0)
	s_barrier
	s_and_saveexec_b64 s[2:3], s[4:5]
	s_cbranch_execz .LBB0_1379
	s_waitcnt vmcnt(0) lgkmcnt(0)
	s_add_u32 s98, s98, 1
	v_mov_b32_e32 v253, 0x12810
	ds_read_b32 v254, v253
	ds_read_b32 v253, v253 offset:4
	s_lshl_b32 s101, s33, 8
	s_add_u32 s99, s101, 5120
	s_waitcnt lgkmcnt(0)
	v_readfirstlane_b32 s100, v254
	v_mov_b32_e32 v254, s99
	v_readfirstlane_b32 s99, v253
	s_nop 0
	v_mov_b32_e32 v253, v254
	v_mov_b32_e32 v254, 1
	global_atomic_add v254, v253, v254, s[44:45] offset:64 sc0
	s_mul_i32 s100, s100, s98
	s_mul_i32 s99, s99, s98
	s_waitcnt vmcnt(0)
	v_add_u32_e32 v254, 1, v254
	v_cmp_ne_u32_e32 vcc, s100, v254
	s_cbranch_vccnz .Lgb_wait_12
	buffer_wbl2 sc1
	s_waitcnt vmcnt(0)
	v_mov_b32_e32 v254, 1
	v_mov_b32_e32 v253, 9216
	global_atomic_add v253, v254, s[44:45] offset:64
	global_atomic_add v253, v254, s[44:45] offset:320
	global_atomic_add v253, v254, s[44:45] offset:576
	global_atomic_add v253, v254, s[44:45] offset:832
	global_atomic_add v253, v254, s[44:45] offset:1088
	global_atomic_add v253, v254, s[44:45] offset:1344
	global_atomic_add v253, v254, s[44:45] offset:1600
	global_atomic_add v253, v254, s[44:45] offset:1856
	v_mov_b32_e32 v253, 11264
	global_atomic_add v253, v254, s[44:45] offset:64
	global_atomic_add v253, v254, s[44:45] offset:320
	global_atomic_add v253, v254, s[44:45] offset:576
	global_atomic_add v253, v254, s[44:45] offset:832
	global_atomic_add v253, v254, s[44:45] offset:1088
	global_atomic_add v253, v254, s[44:45] offset:1344
	global_atomic_add v253, v254, s[44:45] offset:1600
	global_atomic_add v253, v254, s[44:45] offset:1856

.LBB0_1379:
	s_or_b64 exec, exec, s[2:3]
	s_mov_b64 s[14:15], s[0:1]
	s_waitcnt lgkmcnt(0)
	s_barrier
	s_getreg_b32 s35, hwreg(HW_REG_XCC_ID, 0, 4)
	s_load_dwordx4 s[8:11], s[14:15], 0x240
	s_load_dwordx2 s[18:19], s[14:15], 0x230
	s_load_dwordx2 s[16:17], s[14:15], 0x218
	s_load_dwordx2 s[12:13], s[14:15], 0xe8
	v_ashrrev_i32_e32 v1, 6, v0
	v_and_b32_e32 v3, 7, v0
	v_lshlrev_b32_e32 v4, 10, v1
	v_and_b32_e32 v44, 63, v0
	v_bfe_u32 v2, v0, 3, 3
	v_cmp_eq_u32_e64 s[2:3], 0, v0
	v_lshlrev_b32_e32 v55, 4, v3
	v_lshl_add_u32 v0, v1, 13, v4
	v_lshlrev_b32_e32 v3, 3, v3
	v_mov_b32_e32 v47, 0
	v_lshlrev_b32_e32 v45, 4, v1
	v_lshl_or_b32 v54, v44, 2, v4
	v_lshl_or_b32 v56, v2, 2, v4
	s_movk_i32 s20, 0x90
	v_mul_u32_u24_e32 v1, 0x90, v44
	v_mul_u32_u24_e32 v4, 0x90, v2
	v_or_b32_e32 v5, v0, v55
	v_lshlrev_b32_e32 v46, 3, v2
	v_lshl_or_b32 v46, v3, 3, v46
	s_mov_b32 s15, 0x20000
	s_brev_b32 s14, 64
	s_waitcnt lgkmcnt(0)
	s_and_b32 s13, s13, 0xffff
	v_mad_u32_u24 v57, v2, s20, v5
	v_lshl_add_u64 v[48:49], s[18:19], 0, v[46:47]
	v_mov_b32_e32 v58, 1
	s_movk_i32 s36, 0x7f
	s_mov_b32 s37, 0
	v_add_u32_e32 v59, v0, v1
	v_add_u32_e32 v60, v5, v4
	v_add_u32_e32 v61, 0x400, v56
	v_mov_b32_e32 v62, 0
	s_branch .LBB0_1381

.LBB0_1385:
	v_mov_b32_e32 v2, v62
	v_add_u32_e32 v0, s35, v2
	v_and_b32_e32 v1, 7, v0
	v_lshlrev_b32_e32 v0, 8, v1
	global_atomic_add v3, v0, v58, s[44:45] offset:1152 sc0
	s_or_b64 s[26:27], s[26:27], exec
	s_or_b64 s[28:29], s[28:29], exec
	s_waitcnt vmcnt(0)
	v_cmp_lt_i32_e32 vcc, s36, v3
	s_and_saveexec_b64 s[30:31], vcc
	s_cbranch_execz .LBB0_1384
	v_mov_b32_e32 v253, 0x12810
	ds_read_b32 v254, v253 offset:4
	ds_read_b32 v253, v253
	s_waitcnt lgkmcnt(0)
	v_lshlrev_b32_e32 v253, 3, v253
	v_xor_b32_e32 v253, s34, v253
	v_xor_b32_e32 v254, 8, v254
	v_or_b32_e32 v253, v253, v254
	v_cmp_eq_u32_e32 vcc, 0, v253
	v_mov_b32_e32 v254, 7
	s_nop 1
	v_cndmask_b32_e32 v253, v2, v254, vcc
	v_cmp_lt_u32_e32 vcc, 6, v253
	s_andn2_b64 s[28:29], s[28:29], exec
	s_and_b64 s[38:39], vcc, exec
	v_add_u32_e32 v62, 1, v2
	s_andn2_b64 s[26:27], s[26:27], exec
	s_or_b64 s[28:29], s[28:29], s[38:39]
	s_branch .LBB0_1384

.LBB0_1393:
	s_waitcnt vmcnt(3)
	ds_write2_b32 v54, v64, v65 offset0:16 offset1:80
	s_waitcnt vmcnt(1)
	ds_write2_b32 v54, v66, v67 offset0:144 offset1:208
	ds_read2_b32 v[200:201], v56 offset0:16 offset1:24
	ds_read2_b32 v[202:203], v56 offset0:32 offset1:40
	ds_read2_b32 v[204:205], v56 offset0:48 offset1:56
	ds_read2_b32 v[206:207], v56 offset0:64 offset1:72
	ds_read2_b32 v[208:209], v56 offset0:80 offset1:88
	ds_read2_b32 v[210:211], v56 offset0:96 offset1:104
	ds_read2_b32 v[212:213], v56 offset0:112 offset1:120
	ds_read2_b32 v[214:215], v56 offset0:128 offset1:136
	s_cmpk_lg_u32 s18, 0xf000
	s_cselect_b64 s[20:21], -1, 0
	v_cndmask_b32_e64 v64, 0, 1, s[20:21]
	v_mov_b32_e32 v65, s37
	v_lshl_add_u64 v[64:65], v[50:51], 0, v[64:65]
	v_lshlrev_b64 v[66:67], 9, v[64:65]
	v_lshl_or_b32 v66, v44, 2, v66
	v_lshl_add_u64 v[88:89], s[10:11], 0, v[66:67]
	v_lshl_add_u64 v[50:51], v[50:51], 0, 1
	s_waitcnt lgkmcnt(7)
	v_lshl_add_u32 v0, v200, 7, v63
	buffer_load_dwordx4 v[68:71], v0, s[12:15], 0 offen sc0
	v_lshl_add_u32 v0, v201, 7, v63
	buffer_load_dwordx4 v[72:75], v0, s[12:15], 0 offen sc0
	ds_read2_b32 v[216:217], v56 offset0:144 offset1:152
	s_waitcnt lgkmcnt(7)
	v_lshl_add_u32 v0, v202, 7, v63
	buffer_load_dwordx4 v[76:79], v0, s[12:15], 0 offen sc0
	v_lshl_add_u32 v0, v203, 7, v63
	buffer_load_dwordx4 v[80:83], v0, s[12:15], 0 offen sc0
	ds_read2_b32 v[218:219], v56 offset0:160 offset1:168
	s_waitcnt lgkmcnt(7)
	v_lshl_add_u32 v0, v204, 7, v63
	buffer_load_dwordx4 v[84:87], v0, s[12:15], 0 offen sc0
	v_lshl_add_u32 v0, v205, 7, v63
	buffer_load_dwordx4 v[40:43], v0, s[12:15], 0 offen sc0
	ds_read2_b32 v[220:221], v56 offset0:176 offset1:184
	s_waitcnt lgkmcnt(7)
	v_lshl_add_u32 v0, v206, 7, v63
	buffer_load_dwordx4 v[36:39], v0, s[12:15], 0 offen sc0
	v_lshl_add_u32 v0, v207, 7, v63
	buffer_load_dwordx4 v[32:35], v0, s[12:15], 0 offen sc0
	ds_read2_b32 v[222:223], v56 offset0:192 offset1:200
	s_waitcnt lgkmcnt(7)
	v_lshl_add_u32 v0, v208, 7, v63
	buffer_load_dwordx4 v[28:31], v0, s[12:15], 0 offen sc0
	v_lshl_add_u32 v0, v209, 7, v63
	buffer_load_dwordx4 v[24:27], v0, s[12:15], 0 offen sc0
	ds_read2_b32 v[224:225], v56 offset0:208 offset1:216
	s_waitcnt lgkmcnt(7)
	v_lshl_add_u32 v0, v210, 7, v63
	buffer_load_dwordx4 v[20:23], v0, s[12:15], 0 offen sc0
	v_lshl_add_u32 v0, v211, 7, v63
	buffer_load_dwordx4 v[16:19], v0, s[12:15], 0 offen sc0
	ds_read2_b32 v[226:227], v56 offset0:224 offset1:232
	s_waitcnt lgkmcnt(7)
	v_lshl_add_u32 v0, v212, 7, v63
	buffer_load_dwordx4 v[12:15], v0, s[12:15], 0 offen sc0
	v_lshl_add_u32 v0, v213, 7, v63
	buffer_load_dwordx4 v[8:11], v0, s[12:15], 0 offen sc0
	ds_read2_b32 v[228:229], v56 offset0:240 offset1:248
	ds_read2_b32 v[230:231], v61 offset1:8
	s_waitcnt lgkmcnt(8)
	v_lshl_add_u32 v0, v214, 7, v63
	buffer_load_dwordx4 v[4:7], v0, s[12:15], 0 offen sc0
	v_lshl_add_u32 v0, v215, 7, v63
	buffer_load_dwordx4 v[0:3], v0, s[12:15], 0 offen sc0
	s_nop 0
	global_load_dword v64, v[88:89], off
	global_load_dword v65, v[88:89], off offset:256
	v_lshl_add_u64 v[88:89], s[8:9], 0, v[66:67]
	global_load_dword v66, v[88:89], off
	global_load_dword v67, v[88:89], off offset:256
	s_waitcnt vmcnt(16)
	s_waitcnt lgkmcnt(0)
	s_waitcnt vmcnt(19)
	v_cvt_scalef32_pk_f32_fp4 v[152:153], v68, 1.0
	v_cvt_scalef32_pk_f32_fp4 v[154:155], v68, 1.0 op_sel:[1,0,0]
	v_cvt_scalef32_pk_f32_fp4 v[156:157], v68, 1.0 op_sel:[0,1,0]
	v_cvt_scalef32_pk_f32_fp4 v[158:159], v68, 1.0 op_sel:[1,1,0]
	v_cvt_scalef32_pk_f32_fp4 v[160:161], v69, 1.0
	v_pk_mul_f32 v[120:121], v[216:217], v[152:153] op_sel_hi:[0,1]
	v_cvt_scalef32_pk_f32_fp4 v[162:163], v69, 1.0 op_sel:[1,0,0]
	v_pk_mul_f32 v[122:123], v[216:217], v[154:155] op_sel_hi:[0,1]
	v_cvt_scalef32_pk_f32_fp4 v[152:153], v69, 1.0 op_sel:[0,1,0]
	v_pk_mul_f32 v[124:125], v[216:217], v[156:157] op_sel_hi:[0,1]
	v_cvt_scalef32_pk_f32_fp4 v[154:155], v69, 1.0 op_sel:[1,1,0]
	v_pk_mul_f32 v[126:127], v[216:217], v[158:159] op_sel_hi:[0,1]
	v_cvt_scalef32_pk_f32_fp4 v[156:157], v70, 1.0
	v_pk_mul_f32 v[128:129], v[216:217], v[160:161] op_sel_hi:[0,1]
	v_cvt_scalef32_pk_f32_fp4 v[158:159], v70, 1.0 op_sel:[1,0,0]
	v_pk_mul_f32 v[130:131], v[216:217], v[162:163] op_sel_hi:[0,1]
	v_cvt_scalef32_pk_f32_fp4 v[160:161], v70, 1.0 op_sel:[0,1,0]
	v_pk_mul_f32 v[132:133], v[216:217], v[152:153] op_sel_hi:[0,1]
	v_cvt_scalef32_pk_f32_fp4 v[162:163], v70, 1.0 op_sel:[1,1,0]
	v_pk_mul_f32 v[134:135], v[216:217], v[154:155] op_sel_hi:[0,1]
	v_cvt_scalef32_pk_f32_fp4 v[152:153], v71, 1.0
	v_pk_mul_f32 v[136:137], v[216:217], v[156:157] op_sel_hi:[0,1]
	v_cvt_scalef32_pk_f32_fp4 v[154:155], v71, 1.0 op_sel:[1,0,0]
	v_pk_mul_f32 v[138:139], v[216:217], v[158:159] op_sel_hi:[0,1]
	v_cvt_scalef32_pk_f32_fp4 v[156:157], v71, 1.0 op_sel:[0,1,0]
	v_pk_mul_f32 v[140:141], v[216:217], v[160:161] op_sel_hi:[0,1]
	v_cvt_scalef32_pk_f32_fp4 v[158:159], v71, 1.0 op_sel:[1,1,0]
	v_pk_mul_f32 v[142:143], v[216:217], v[162:163] op_sel_hi:[0,1]
	v_pk_mul_f32 v[144:145], v[216:217], v[152:153] op_sel_hi:[0,1]
	v_pk_mul_f32 v[146:147], v[216:217], v[154:155] op_sel_hi:[0,1]
	v_pk_mul_f32 v[148:149], v[216:217], v[156:157] op_sel_hi:[0,1]
	v_pk_mul_f32 v[150:151], v[216:217], v[158:159] op_sel_hi:[0,1]
	s_waitcnt vmcnt(18)
	v_cvt_scalef32_pk_f32_fp4 v[152:153], v72, 1.0
	v_cvt_scalef32_pk_f32_fp4 v[154:155], v72, 1.0 op_sel:[1,0,0]
	v_cvt_scalef32_pk_f32_fp4 v[156:157], v72, 1.0 op_sel:[0,1,0]
	v_cvt_scalef32_pk_f32_fp4 v[158:159], v72, 1.0 op_sel:[1,1,0]
	v_cvt_scalef32_pk_f32_fp4 v[160:161], v73, 1.0
	v_pk_fma_f32 v[120:121], v[216:217], v[152:153], v[120:121] op_sel:[1,0,0] op_sel_hi:[1,1,1]
	v_cvt_scalef32_pk_f32_fp4 v[162:163], v73, 1.0 op_sel:[1,0,0]
	v_pk_fma_f32 v[122:123], v[216:217], v[154:155], v[122:123] op_sel:[1,0,0] op_sel_hi:[1,1,1]
	v_cvt_scalef32_pk_f32_fp4 v[152:153], v73, 1.0 op_sel:[0,1,0]
	v_pk_fma_f32 v[124:125], v[216:217], v[156:157], v[124:125] op_sel:[1,0,0] op_sel_hi:[1,1,1]
	v_cvt_scalef32_pk_f32_fp4 v[154:155], v73, 1.0 op_sel:[1,1,0]
	v_pk_fma_f32 v[126:127], v[216:217], v[158:159], v[126:127] op_sel:[1,0,0] op_sel_hi:[1,1,1]
	v_cvt_scalef32_pk_f32_fp4 v[156:157], v74, 1.0
	v_pk_fma_f32 v[128:129], v[216:217], v[160:161], v[128:129] op_sel:[1,0,0] op_sel_hi:[1,1,1]
	v_cvt_scalef32_pk_f32_fp4 v[158:159], v74, 1.0 op_sel:[1,0,0]
	v_pk_fma_f32 v[130:131], v[216:217], v[162:163], v[130:131] op_sel:[1,0,0] op_sel_hi:[1,1,1]
	v_cvt_scalef32_pk_f32_fp4 v[160:161], v74, 1.0 op_sel:[0,1,0]
	v_pk_fma_f32 v[132:133], v[216:217], v[152:153], v[132:133] op_sel:[1,0,0] op_sel_hi:[1,1,1]
	v_cvt_scalef32_pk_f32_fp4 v[162:163], v74, 1.0 op_sel:[1,1,0]
	v_pk_fma_f32 v[134:135], v[216:217], v[154:155], v[134:135] op_sel:[1,0,0] op_sel_hi:[1,1,1]
	v_cvt_scalef32_pk_f32_fp4 v[152:153], v75, 1.0
	v_pk_fma_f32 v[136:137], v[216:217], v[156:157], v[136:137] op_sel:[1,0,0] op_sel_hi:[1,1,1]
	v_cvt_scalef32_pk_f32_fp4 v[154:155], v75, 1.0 op_sel:[1,0,0]
	v_pk_fma_f32 v[138:139], v[216:217], v[158:159], v[138:139] op_sel:[1,0,0] op_sel_hi:[1,1,1]
	v_cvt_scalef32_pk_f32_fp4 v[156:157], v75, 1.0 op_sel:[0,1,0]
	v_pk_fma_f32 v[140:141], v[216:217], v[160:161], v[140:141] op_sel:[1,0,0] op_sel_hi:[1,1,1]
	v_cvt_scalef32_pk_f32_fp4 v[158:159], v75, 1.0 op_sel:[1,1,0]
	v_pk_fma_f32 v[142:143], v[216:217], v[162:163], v[142:143] op_sel:[1,0,0] op_sel_hi:[1,1,1]
	v_pk_fma_f32 v[144:145], v[216:217], v[152:153], v[144:145] op_sel:[1,0,0] op_sel_hi:[1,1,1]
	v_pk_fma_f32 v[146:147], v[216:217], v[154:155], v[146:147] op_sel:[1,0,0] op_sel_hi:[1,1,1]
	v_pk_fma_f32 v[148:149], v[216:217], v[156:157], v[148:149] op_sel:[1,0,0] op_sel_hi:[1,1,1]
	v_pk_fma_f32 v[150:151], v[216:217], v[158:159], v[150:151] op_sel:[1,0,0] op_sel_hi:[1,1,1]
	s_waitcnt vmcnt(17)
	v_cvt_scalef32_pk_f32_fp4 v[152:153], v76, 1.0
	v_cvt_scalef32_pk_f32_fp4 v[154:155], v76, 1.0 op_sel:[1,0,0]
	v_cvt_scalef32_pk_f32_fp4 v[156:157], v76, 1.0 op_sel:[0,1,0]
	v_cvt_scalef32_pk_f32_fp4 v[158:159], v76, 1.0 op_sel:[1,1,0]
	v_cvt_scalef32_pk_f32_fp4 v[160:161], v77, 1.0
	v_pk_fma_f32 v[120:121], v[218:219], v[152:153], v[120:121] op_sel_hi:[0,1,1]
	v_cvt_scalef32_pk_f32_fp4 v[162:163], v77, 1.0 op_sel:[1,0,0]
	v_pk_fma_f32 v[122:123], v[218:219], v[154:155], v[122:123] op_sel_hi:[0,1,1]
	v_cvt_scalef32_pk_f32_fp4 v[152:153], v77, 1.0 op_sel:[0,1,0]
	v_pk_fma_f32 v[124:125], v[218:219], v[156:157], v[124:125] op_sel_hi:[0,1,1]
	v_cvt_scalef32_pk_f32_fp4 v[154:155], v77, 1.0 op_sel:[1,1,0]
	v_pk_fma_f32 v[126:127], v[218:219], v[158:159], v[126:127] op_sel_hi:[0,1,1]
	v_cvt_scalef32_pk_f32_fp4 v[156:157], v78, 1.0
	v_pk_fma_f32 v[128:129], v[218:219], v[160:161], v[128:129] op_sel_hi:[0,1,1]
	v_cvt_scalef32_pk_f32_fp4 v[158:159], v78, 1.0 op_sel:[1,0,0]
	v_pk_fma_f32 v[130:131], v[218:219], v[162:163], v[130:131] op_sel_hi:[0,1,1]
	v_cvt_scalef32_pk_f32_fp4 v[160:161], v78, 1.0 op_sel:[0,1,0]
	v_pk_fma_f32 v[132:133], v[218:219], v[152:153], v[132:133] op_sel_hi:[0,1,1]
	v_cvt_scalef32_pk_f32_fp4 v[162:163], v78, 1.0 op_sel:[1,1,0]
	v_pk_fma_f32 v[134:135], v[218:219], v[154:155], v[134:135] op_sel_hi:[0,1,1]
	v_cvt_scalef32_pk_f32_fp4 v[152:153], v79, 1.0
	v_pk_fma_f32 v[136:137], v[218:219], v[156:157], v[136:137] op_sel_hi:[0,1,1]
	v_cvt_scalef32_pk_f32_fp4 v[154:155], v79, 1.0 op_sel:[1,0,0]
	v_pk_fma_f32 v[138:139], v[218:219], v[158:159], v[138:139] op_sel_hi:[0,1,1]
	v_cvt_scalef32_pk_f32_fp4 v[156:157], v79, 1.0 op_sel:[0,1,0]
	v_pk_fma_f32 v[140:141], v[218:219], v[160:161], v[140:141] op_sel_hi:[0,1,1]
	v_cvt_scalef32_pk_f32_fp4 v[158:159], v79, 1.0 op_sel:[1,1,0]
	v_pk_fma_f32 v[142:143], v[218:219], v[162:163], v[142:143] op_sel_hi:[0,1,1]
	v_pk_fma_f32 v[144:145], v[218:219], v[152:153], v[144:145] op_sel_hi:[0,1,1]
	v_pk_fma_f32 v[146:147], v[218:219], v[154:155], v[146:147] op_sel_hi:[0,1,1]
	v_pk_fma_f32 v[148:149], v[218:219], v[156:157], v[148:149] op_sel_hi:[0,1,1]
	v_pk_fma_f32 v[150:151], v[218:219], v[158:159], v[150:151] op_sel_hi:[0,1,1]
	s_waitcnt vmcnt(16)
	v_cvt_scalef32_pk_f32_fp4 v[152:153], v80, 1.0
	v_cvt_scalef32_pk_f32_fp4 v[154:155], v80, 1.0 op_sel:[1,0,0]
	v_cvt_scalef32_pk_f32_fp4 v[156:157], v80, 1.0 op_sel:[0,1,0]
	v_cvt_scalef32_pk_f32_fp4 v[158:159], v80, 1.0 op_sel:[1,1,0]
	v_cvt_scalef32_pk_f32_fp4 v[160:161], v81, 1.0
	v_pk_fma_f32 v[120:121], v[218:219], v[152:153], v[120:121] op_sel:[1,0,0] op_sel_hi:[1,1,1]
	v_cvt_scalef32_pk_f32_fp4 v[162:163], v81, 1.0 op_sel:[1,0,0]
	v_pk_fma_f32 v[122:123], v[218:219], v[154:155], v[122:123] op_sel:[1,0,0] op_sel_hi:[1,1,1]
	v_cvt_scalef32_pk_f32_fp4 v[152:153], v81, 1.0 op_sel:[0,1,0]
	v_pk_fma_f32 v[124:125], v[218:219], v[156:157], v[124:125] op_sel:[1,0,0] op_sel_hi:[1,1,1]
	v_cvt_scalef32_pk_f32_fp4 v[154:155], v81, 1.0 op_sel:[1,1,0]
	v_pk_fma_f32 v[126:127], v[218:219], v[158:159], v[126:127] op_sel:[1,0,0] op_sel_hi:[1,1,1]
	v_cvt_scalef32_pk_f32_fp4 v[156:157], v82, 1.0
	v_pk_fma_f32 v[128:129], v[218:219], v[160:161], v[128:129] op_sel:[1,0,0] op_sel_hi:[1,1,1]
	v_cvt_scalef32_pk_f32_fp4 v[158:159], v82, 1.0 op_sel:[1,0,0]
	v_pk_fma_f32 v[130:131], v[218:219], v[162:163], v[130:131] op_sel:[1,0,0] op_sel_hi:[1,1,1]
	v_cvt_scalef32_pk_f32_fp4 v[160:161], v82, 1.0 op_sel:[0,1,0]
	v_pk_fma_f32 v[132:133], v[218:219], v[152:153], v[132:133] op_sel:[1,0,0] op_sel_hi:[1,1,1]
	v_cvt_scalef32_pk_f32_fp4 v[162:163], v82, 1.0 op_sel:[1,1,0]
	v_pk_fma_f32 v[134:135], v[218:219], v[154:155], v[134:135] op_sel:[1,0,0] op_sel_hi:[1,1,1]
	v_cvt_scalef32_pk_f32_fp4 v[152:153], v83, 1.0
	v_pk_fma_f32 v[136:137], v[218:219], v[156:157], v[136:137] op_sel:[1,0,0] op_sel_hi:[1,1,1]
	v_cvt_scalef32_pk_f32_fp4 v[154:155], v83, 1.0 op_sel:[1,0,0]
	v_pk_fma_f32 v[138:139], v[218:219], v[158:159], v[138:139] op_sel:[1,0,0] op_sel_hi:[1,1,1]
	v_cvt_scalef32_pk_f32_fp4 v[156:157], v83, 1.0 op_sel:[0,1,0]
	v_pk_fma_f32 v[140:141], v[218:219], v[160:161], v[140:141] op_sel:[1,0,0] op_sel_hi:[1,1,1]
	v_cvt_scalef32_pk_f32_fp4 v[158:159], v83, 1.0 op_sel:[1,1,0]
	v_pk_fma_f32 v[142:143], v[218:219], v[162:163], v[142:143] op_sel:[1,0,0] op_sel_hi:[1,1,1]
	v_pk_fma_f32 v[144:145], v[218:219], v[152:153], v[144:145] op_sel:[1,0,0] op_sel_hi:[1,1,1]
	v_pk_fma_f32 v[146:147], v[218:219], v[154:155], v[146:147] op_sel:[1,0,0] op_sel_hi:[1,1,1]
	v_pk_fma_f32 v[148:149], v[218:219], v[156:157], v[148:149] op_sel:[1,0,0] op_sel_hi:[1,1,1]
	v_pk_fma_f32 v[150:151], v[218:219], v[158:159], v[150:151] op_sel:[1,0,0] op_sel_hi:[1,1,1]
	s_waitcnt vmcnt(15)
	v_cvt_scalef32_pk_f32_fp4 v[152:153], v84, 1.0
	v_cvt_scalef32_pk_f32_fp4 v[154:155], v84, 1.0 op_sel:[1,0,0]
	v_cvt_scalef32_pk_f32_fp4 v[156:157], v84, 1.0 op_sel:[0,1,0]
	v_cvt_scalef32_pk_f32_fp4 v[158:159], v84, 1.0 op_sel:[1,1,0]
	v_cvt_scalef32_pk_f32_fp4 v[160:161], v85, 1.0
	v_pk_fma_f32 v[120:121], v[220:221], v[152:153], v[120:121] op_sel_hi:[0,1,1]
	v_cvt_scalef32_pk_f32_fp4 v[162:163], v85, 1.0 op_sel:[1,0,0]
	v_pk_fma_f32 v[122:123], v[220:221], v[154:155], v[122:123] op_sel_hi:[0,1,1]
	v_cvt_scalef32_pk_f32_fp4 v[152:153], v85, 1.0 op_sel:[0,1,0]
	v_pk_fma_f32 v[124:125], v[220:221], v[156:157], v[124:125] op_sel_hi:[0,1,1]
	v_cvt_scalef32_pk_f32_fp4 v[154:155], v85, 1.0 op_sel:[1,1,0]
	v_pk_fma_f32 v[126:127], v[220:221], v[158:159], v[126:127] op_sel_hi:[0,1,1]
	v_cvt_scalef32_pk_f32_fp4 v[156:157], v86, 1.0
	v_pk_fma_f32 v[128:129], v[220:221], v[160:161], v[128:129] op_sel_hi:[0,1,1]
	v_cvt_scalef32_pk_f32_fp4 v[158:159], v86, 1.0 op_sel:[1,0,0]
	v_pk_fma_f32 v[130:131], v[220:221], v[162:163], v[130:131] op_sel_hi:[0,1,1]
	v_cvt_scalef32_pk_f32_fp4 v[160:161], v86, 1.0 op_sel:[0,1,0]
	v_pk_fma_f32 v[132:133], v[220:221], v[152:153], v[132:133] op_sel_hi:[0,1,1]
	v_cvt_scalef32_pk_f32_fp4 v[162:163], v86, 1.0 op_sel:[1,1,0]
	v_pk_fma_f32 v[134:135], v[220:221], v[154:155], v[134:135] op_sel_hi:[0,1,1]
	v_cvt_scalef32_pk_f32_fp4 v[152:153], v87, 1.0
	v_pk_fma_f32 v[136:137], v[220:221], v[156:157], v[136:137] op_sel_hi:[0,1,1]
	v_cvt_scalef32_pk_f32_fp4 v[154:155], v87, 1.0 op_sel:[1,0,0]
	v_pk_fma_f32 v[138:139], v[220:221], v[158:159], v[138:139] op_sel_hi:[0,1,1]
	v_cvt_scalef32_pk_f32_fp4 v[156:157], v87, 1.0 op_sel:[0,1,0]
	v_pk_fma_f32 v[140:141], v[220:221], v[160:161], v[140:141] op_sel_hi:[0,1,1]
	v_cvt_scalef32_pk_f32_fp4 v[158:159], v87, 1.0 op_sel:[1,1,0]
	v_pk_fma_f32 v[142:143], v[220:221], v[162:163], v[142:143] op_sel_hi:[0,1,1]
	v_pk_fma_f32 v[144:145], v[220:221], v[152:153], v[144:145] op_sel_hi:[0,1,1]
	v_pk_fma_f32 v[146:147], v[220:221], v[154:155], v[146:147] op_sel_hi:[0,1,1]
	v_pk_fma_f32 v[148:149], v[220:221], v[156:157], v[148:149] op_sel_hi:[0,1,1]
	v_pk_fma_f32 v[150:151], v[220:221], v[158:159], v[150:151] op_sel_hi:[0,1,1]
	s_waitcnt vmcnt(14)
	v_cvt_scalef32_pk_f32_fp4 v[152:153], v40, 1.0
	v_cvt_scalef32_pk_f32_fp4 v[154:155], v40, 1.0 op_sel:[1,0,0]
	v_cvt_scalef32_pk_f32_fp4 v[156:157], v40, 1.0 op_sel:[0,1,0]
	v_cvt_scalef32_pk_f32_fp4 v[158:159], v40, 1.0 op_sel:[1,1,0]
	v_cvt_scalef32_pk_f32_fp4 v[160:161], v41, 1.0
	v_pk_fma_f32 v[120:121], v[220:221], v[152:153], v[120:121] op_sel:[1,0,0] op_sel_hi:[1,1,1]
	v_cvt_scalef32_pk_f32_fp4 v[162:163], v41, 1.0 op_sel:[1,0,0]
	v_pk_fma_f32 v[122:123], v[220:221], v[154:155], v[122:123] op_sel:[1,0,0] op_sel_hi:[1,1,1]
	v_cvt_scalef32_pk_f32_fp4 v[152:153], v41, 1.0 op_sel:[0,1,0]
	v_pk_fma_f32 v[124:125], v[220:221], v[156:157], v[124:125] op_sel:[1,0,0] op_sel_hi:[1,1,1]
	v_cvt_scalef32_pk_f32_fp4 v[154:155], v41, 1.0 op_sel:[1,1,0]
	v_pk_fma_f32 v[126:127], v[220:221], v[158:159], v[126:127] op_sel:[1,0,0] op_sel_hi:[1,1,1]
	v_cvt_scalef32_pk_f32_fp4 v[156:157], v42, 1.0
	v_pk_fma_f32 v[128:129], v[220:221], v[160:161], v[128:129] op_sel:[1,0,0] op_sel_hi:[1,1,1]
	v_cvt_scalef32_pk_f32_fp4 v[158:159], v42, 1.0 op_sel:[1,0,0]
	v_pk_fma_f32 v[130:131], v[220:221], v[162:163], v[130:131] op_sel:[1,0,0] op_sel_hi:[1,1,1]
	v_cvt_scalef32_pk_f32_fp4 v[160:161], v42, 1.0 op_sel:[0,1,0]
	v_pk_fma_f32 v[132:133], v[220:221], v[152:153], v[132:133] op_sel:[1,0,0] op_sel_hi:[1,1,1]
	v_cvt_scalef32_pk_f32_fp4 v[162:163], v42, 1.0 op_sel:[1,1,0]
	v_pk_fma_f32 v[134:135], v[220:221], v[154:155], v[134:135] op_sel:[1,0,0] op_sel_hi:[1,1,1]
	v_cvt_scalef32_pk_f32_fp4 v[152:153], v43, 1.0
	v_pk_fma_f32 v[136:137], v[220:221], v[156:157], v[136:137] op_sel:[1,0,0] op_sel_hi:[1,1,1]
	v_cvt_scalef32_pk_f32_fp4 v[154:155], v43, 1.0 op_sel:[1,0,0]
	v_pk_fma_f32 v[138:139], v[220:221], v[158:159], v[138:139] op_sel:[1,0,0] op_sel_hi:[1,1,1]
	v_cvt_scalef32_pk_f32_fp4 v[156:157], v43, 1.0 op_sel:[0,1,0]
	v_pk_fma_f32 v[140:141], v[220:221], v[160:161], v[140:141] op_sel:[1,0,0] op_sel_hi:[1,1,1]
	v_cvt_scalef32_pk_f32_fp4 v[158:159], v43, 1.0 op_sel:[1,1,0]
	v_pk_fma_f32 v[142:143], v[220:221], v[162:163], v[142:143] op_sel:[1,0,0] op_sel_hi:[1,1,1]
	v_pk_fma_f32 v[144:145], v[220:221], v[152:153], v[144:145] op_sel:[1,0,0] op_sel_hi:[1,1,1]
	v_pk_fma_f32 v[146:147], v[220:221], v[154:155], v[146:147] op_sel:[1,0,0] op_sel_hi:[1,1,1]
	v_pk_fma_f32 v[148:149], v[220:221], v[156:157], v[148:149] op_sel:[1,0,0] op_sel_hi:[1,1,1]
	v_pk_fma_f32 v[150:151], v[220:221], v[158:159], v[150:151] op_sel:[1,0,0] op_sel_hi:[1,1,1]
	s_waitcnt vmcnt(13)
	v_cvt_scalef32_pk_f32_fp4 v[152:153], v36, 1.0
	v_cvt_scalef32_pk_f32_fp4 v[154:155], v36, 1.0 op_sel:[1,0,0]
	v_cvt_scalef32_pk_f32_fp4 v[156:157], v36, 1.0 op_sel:[0,1,0]
	v_cvt_scalef32_pk_f32_fp4 v[158:159], v36, 1.0 op_sel:[1,1,0]
	v_cvt_scalef32_pk_f32_fp4 v[160:161], v37, 1.0
	v_pk_fma_f32 v[120:121], v[222:223], v[152:153], v[120:121] op_sel_hi:[0,1,1]
	v_cvt_scalef32_pk_f32_fp4 v[162:163], v37, 1.0 op_sel:[1,0,0]
	v_pk_fma_f32 v[122:123], v[222:223], v[154:155], v[122:123] op_sel_hi:[0,1,1]
	v_cvt_scalef32_pk_f32_fp4 v[152:153], v37, 1.0 op_sel:[0,1,0]
	v_pk_fma_f32 v[124:125], v[222:223], v[156:157], v[124:125] op_sel_hi:[0,1,1]
	v_cvt_scalef32_pk_f32_fp4 v[154:155], v37, 1.0 op_sel:[1,1,0]
	v_pk_fma_f32 v[126:127], v[222:223], v[158:159], v[126:127] op_sel_hi:[0,1,1]
	v_cvt_scalef32_pk_f32_fp4 v[156:157], v38, 1.0
	v_pk_fma_f32 v[128:129], v[222:223], v[160:161], v[128:129] op_sel_hi:[0,1,1]
	v_cvt_scalef32_pk_f32_fp4 v[158:159], v38, 1.0 op_sel:[1,0,0]
	v_pk_fma_f32 v[130:131], v[222:223], v[162:163], v[130:131] op_sel_hi:[0,1,1]
	v_cvt_scalef32_pk_f32_fp4 v[160:161], v38, 1.0 op_sel:[0,1,0]
	v_pk_fma_f32 v[132:133], v[222:223], v[152:153], v[132:133] op_sel_hi:[0,1,1]
	v_cvt_scalef32_pk_f32_fp4 v[162:163], v38, 1.0 op_sel:[1,1,0]
	v_pk_fma_f32 v[134:135], v[222:223], v[154:155], v[134:135] op_sel_hi:[0,1,1]
	v_cvt_scalef32_pk_f32_fp4 v[152:153], v39, 1.0
	v_pk_fma_f32 v[136:137], v[222:223], v[156:157], v[136:137] op_sel_hi:[0,1,1]
	v_cvt_scalef32_pk_f32_fp4 v[154:155], v39, 1.0 op_sel:[1,0,0]
	v_pk_fma_f32 v[138:139], v[222:223], v[158:159], v[138:139] op_sel_hi:[0,1,1]
	v_cvt_scalef32_pk_f32_fp4 v[156:157], v39, 1.0 op_sel:[0,1,0]
	v_pk_fma_f32 v[140:141], v[222:223], v[160:161], v[140:141] op_sel_hi:[0,1,1]
	v_cvt_scalef32_pk_f32_fp4 v[158:159], v39, 1.0 op_sel:[1,1,0]
	v_pk_fma_f32 v[142:143], v[222:223], v[162:163], v[142:143] op_sel_hi:[0,1,1]
	v_pk_fma_f32 v[144:145], v[222:223], v[152:153], v[144:145] op_sel_hi:[0,1,1]
	v_pk_fma_f32 v[146:147], v[222:223], v[154:155], v[146:147] op_sel_hi:[0,1,1]
	v_pk_fma_f32 v[148:149], v[222:223], v[156:157], v[148:149] op_sel_hi:[0,1,1]
	v_pk_fma_f32 v[150:151], v[222:223], v[158:159], v[150:151] op_sel_hi:[0,1,1]
	s_waitcnt vmcnt(12)
	v_cvt_scalef32_pk_f32_fp4 v[152:153], v32, 1.0
	v_cvt_scalef32_pk_f32_fp4 v[154:155], v32, 1.0 op_sel:[1,0,0]
	v_cvt_scalef32_pk_f32_fp4 v[156:157], v32, 1.0 op_sel:[0,1,0]
	v_cvt_scalef32_pk_f32_fp4 v[158:159], v32, 1.0 op_sel:[1,1,0]
	v_cvt_scalef32_pk_f32_fp4 v[160:161], v33, 1.0
	v_pk_fma_f32 v[120:121], v[222:223], v[152:153], v[120:121] op_sel:[1,0,0] op_sel_hi:[1,1,1]
	v_cvt_scalef32_pk_f32_fp4 v[162:163], v33, 1.0 op_sel:[1,0,0]
	v_pk_fma_f32 v[122:123], v[222:223], v[154:155], v[122:123] op_sel:[1,0,0] op_sel_hi:[1,1,1]
	v_cvt_scalef32_pk_f32_fp4 v[152:153], v33, 1.0 op_sel:[0,1,0]
	v_pk_fma_f32 v[124:125], v[222:223], v[156:157], v[124:125] op_sel:[1,0,0] op_sel_hi:[1,1,1]
	v_cvt_scalef32_pk_f32_fp4 v[154:155], v33, 1.0 op_sel:[1,1,0]
	v_pk_fma_f32 v[126:127], v[222:223], v[158:159], v[126:127] op_sel:[1,0,0] op_sel_hi:[1,1,1]
	v_cvt_scalef32_pk_f32_fp4 v[156:157], v34, 1.0
	v_pk_fma_f32 v[128:129], v[222:223], v[160:161], v[128:129] op_sel:[1,0,0] op_sel_hi:[1,1,1]
	v_cvt_scalef32_pk_f32_fp4 v[158:159], v34, 1.0 op_sel:[1,0,0]
	v_pk_fma_f32 v[130:131], v[222:223], v[162:163], v[130:131] op_sel:[1,0,0] op_sel_hi:[1,1,1]
	v_cvt_scalef32_pk_f32_fp4 v[160:161], v34, 1.0 op_sel:[0,1,0]
	v_pk_fma_f32 v[132:133], v[222:223], v[152:153], v[132:133] op_sel:[1,0,0] op_sel_hi:[1,1,1]
	v_cvt_scalef32_pk_f32_fp4 v[162:163], v34, 1.0 op_sel:[1,1,0]
	v_pk_fma_f32 v[134:135], v[222:223], v[154:155], v[134:135] op_sel:[1,0,0] op_sel_hi:[1,1,1]
	v_cvt_scalef32_pk_f32_fp4 v[152:153], v35, 1.0
	v_pk_fma_f32 v[136:137], v[222:223], v[156:157], v[136:137] op_sel:[1,0,0] op_sel_hi:[1,1,1]
	v_cvt_scalef32_pk_f32_fp4 v[154:155], v35, 1.0 op_sel:[1,0,0]
	v_pk_fma_f32 v[138:139], v[222:223], v[158:159], v[138:139] op_sel:[1,0,0] op_sel_hi:[1,1,1]
	v_cvt_scalef32_pk_f32_fp4 v[156:157], v35, 1.0 op_sel:[0,1,0]
	v_pk_fma_f32 v[140:141], v[222:223], v[160:161], v[140:141] op_sel:[1,0,0] op_sel_hi:[1,1,1]
	v_cvt_scalef32_pk_f32_fp4 v[158:159], v35, 1.0 op_sel:[1,1,0]
	v_pk_fma_f32 v[142:143], v[222:223], v[162:163], v[142:143] op_sel:[1,0,0] op_sel_hi:[1,1,1]
	v_pk_fma_f32 v[144:145], v[222:223], v[152:153], v[144:145] op_sel:[1,0,0] op_sel_hi:[1,1,1]
	v_pk_fma_f32 v[146:147], v[222:223], v[154:155], v[146:147] op_sel:[1,0,0] op_sel_hi:[1,1,1]
	v_pk_fma_f32 v[148:149], v[222:223], v[156:157], v[148:149] op_sel:[1,0,0] op_sel_hi:[1,1,1]
	v_pk_fma_f32 v[150:151], v[222:223], v[158:159], v[150:151] op_sel:[1,0,0] op_sel_hi:[1,1,1]
	s_waitcnt vmcnt(11)
	v_cvt_scalef32_pk_f32_fp4 v[152:153], v28, 1.0
	v_cvt_scalef32_pk_f32_fp4 v[154:155], v28, 1.0 op_sel:[1,0,0]
	v_cvt_scalef32_pk_f32_fp4 v[156:157], v28, 1.0 op_sel:[0,1,0]
	v_cvt_scalef32_pk_f32_fp4 v[158:159], v28, 1.0 op_sel:[1,1,0]
	v_cvt_scalef32_pk_f32_fp4 v[160:161], v29, 1.0
	v_pk_fma_f32 v[120:121], v[224:225], v[152:153], v[120:121] op_sel_hi:[0,1,1]
	v_cvt_scalef32_pk_f32_fp4 v[162:163], v29, 1.0 op_sel:[1,0,0]
	v_pk_fma_f32 v[122:123], v[224:225], v[154:155], v[122:123] op_sel_hi:[0,1,1]
	v_cvt_scalef32_pk_f32_fp4 v[152:153], v29, 1.0 op_sel:[0,1,0]
	v_pk_fma_f32 v[124:125], v[224:225], v[156:157], v[124:125] op_sel_hi:[0,1,1]
	v_cvt_scalef32_pk_f32_fp4 v[154:155], v29, 1.0 op_sel:[1,1,0]
	v_pk_fma_f32 v[126:127], v[224:225], v[158:159], v[126:127] op_sel_hi:[0,1,1]
	v_cvt_scalef32_pk_f32_fp4 v[156:157], v30, 1.0
	v_pk_fma_f32 v[128:129], v[224:225], v[160:161], v[128:129] op_sel_hi:[0,1,1]
	v_cvt_scalef32_pk_f32_fp4 v[158:159], v30, 1.0 op_sel:[1,0,0]
	v_pk_fma_f32 v[130:131], v[224:225], v[162:163], v[130:131] op_sel_hi:[0,1,1]
	v_cvt_scalef32_pk_f32_fp4 v[160:161], v30, 1.0 op_sel:[0,1,0]
	v_pk_fma_f32 v[132:133], v[224:225], v[152:153], v[132:133] op_sel_hi:[0,1,1]
	v_cvt_scalef32_pk_f32_fp4 v[162:163], v30, 1.0 op_sel:[1,1,0]
	v_pk_fma_f32 v[134:135], v[224:225], v[154:155], v[134:135] op_sel_hi:[0,1,1]
	v_cvt_scalef32_pk_f32_fp4 v[152:153], v31, 1.0
	v_pk_fma_f32 v[136:137], v[224:225], v[156:157], v[136:137] op_sel_hi:[0,1,1]
	v_cvt_scalef32_pk_f32_fp4 v[154:155], v31, 1.0 op_sel:[1,0,0]
	v_pk_fma_f32 v[138:139], v[224:225], v[158:159], v[138:139] op_sel_hi:[0,1,1]
	v_cvt_scalef32_pk_f32_fp4 v[156:157], v31, 1.0 op_sel:[0,1,0]
	v_pk_fma_f32 v[140:141], v[224:225], v[160:161], v[140:141] op_sel_hi:[0,1,1]
	v_cvt_scalef32_pk_f32_fp4 v[158:159], v31, 1.0 op_sel:[1,1,0]
	v_pk_fma_f32 v[142:143], v[224:225], v[162:163], v[142:143] op_sel_hi:[0,1,1]
	v_pk_fma_f32 v[144:145], v[224:225], v[152:153], v[144:145] op_sel_hi:[0,1,1]
	v_pk_fma_f32 v[146:147], v[224:225], v[154:155], v[146:147] op_sel_hi:[0,1,1]
	v_pk_fma_f32 v[148:149], v[224:225], v[156:157], v[148:149] op_sel_hi:[0,1,1]
	v_pk_fma_f32 v[150:151], v[224:225], v[158:159], v[150:151] op_sel_hi:[0,1,1]
	s_waitcnt vmcnt(10)
	v_cvt_scalef32_pk_f32_fp4 v[152:153], v24, 1.0
	v_cvt_scalef32_pk_f32_fp4 v[154:155], v24, 1.0 op_sel:[1,0,0]
	v_cvt_scalef32_pk_f32_fp4 v[156:157], v24, 1.0 op_sel:[0,1,0]
	v_cvt_scalef32_pk_f32_fp4 v[158:159], v24, 1.0 op_sel:[1,1,0]
	v_cvt_scalef32_pk_f32_fp4 v[160:161], v25, 1.0
	v_pk_fma_f32 v[120:121], v[224:225], v[152:153], v[120:121] op_sel:[1,0,0] op_sel_hi:[1,1,1]
	v_cvt_scalef32_pk_f32_fp4 v[162:163], v25, 1.0 op_sel:[1,0,0]
	v_pk_fma_f32 v[122:123], v[224:225], v[154:155], v[122:123] op_sel:[1,0,0] op_sel_hi:[1,1,1]
	v_cvt_scalef32_pk_f32_fp4 v[152:153], v25, 1.0 op_sel:[0,1,0]
	v_pk_fma_f32 v[124:125], v[224:225], v[156:157], v[124:125] op_sel:[1,0,0] op_sel_hi:[1,1,1]
	v_cvt_scalef32_pk_f32_fp4 v[154:155], v25, 1.0 op_sel:[1,1,0]
	v_pk_fma_f32 v[126:127], v[224:225], v[158:159], v[126:127] op_sel:[1,0,0] op_sel_hi:[1,1,1]
	v_cvt_scalef32_pk_f32_fp4 v[156:157], v26, 1.0
	v_pk_fma_f32 v[128:129], v[224:225], v[160:161], v[128:129] op_sel:[1,0,0] op_sel_hi:[1,1,1]
	v_cvt_scalef32_pk_f32_fp4 v[158:159], v26, 1.0 op_sel:[1,0,0]
	v_pk_fma_f32 v[130:131], v[224:225], v[162:163], v[130:131] op_sel:[1,0,0] op_sel_hi:[1,1,1]
	v_cvt_scalef32_pk_f32_fp4 v[160:161], v26, 1.0 op_sel:[0,1,0]
	v_pk_fma_f32 v[132:133], v[224:225], v[152:153], v[132:133] op_sel:[1,0,0] op_sel_hi:[1,1,1]
	v_cvt_scalef32_pk_f32_fp4 v[162:163], v26, 1.0 op_sel:[1,1,0]
	v_pk_fma_f32 v[134:135], v[224:225], v[154:155], v[134:135] op_sel:[1,0,0] op_sel_hi:[1,1,1]
	v_cvt_scalef32_pk_f32_fp4 v[152:153], v27, 1.0
	v_pk_fma_f32 v[136:137], v[224:225], v[156:157], v[136:137] op_sel:[1,0,0] op_sel_hi:[1,1,1]
	v_cvt_scalef32_pk_f32_fp4 v[154:155], v27, 1.0 op_sel:[1,0,0]
	v_pk_fma_f32 v[138:139], v[224:225], v[158:159], v[138:139] op_sel:[1,0,0] op_sel_hi:[1,1,1]
	v_cvt_scalef32_pk_f32_fp4 v[156:157], v27, 1.0 op_sel:[0,1,0]
	v_pk_fma_f32 v[140:141], v[224:225], v[160:161], v[140:141] op_sel:[1,0,0] op_sel_hi:[1,1,1]
	v_cvt_scalef32_pk_f32_fp4 v[158:159], v27, 1.0 op_sel:[1,1,0]
	v_pk_fma_f32 v[142:143], v[224:225], v[162:163], v[142:143] op_sel:[1,0,0] op_sel_hi:[1,1,1]
	v_pk_fma_f32 v[144:145], v[224:225], v[152:153], v[144:145] op_sel:[1,0,0] op_sel_hi:[1,1,1]
	v_pk_fma_f32 v[146:147], v[224:225], v[154:155], v[146:147] op_sel:[1,0,0] op_sel_hi:[1,1,1]
	v_pk_fma_f32 v[148:149], v[224:225], v[156:157], v[148:149] op_sel:[1,0,0] op_sel_hi:[1,1,1]
	v_pk_fma_f32 v[150:151], v[224:225], v[158:159], v[150:151] op_sel:[1,0,0] op_sel_hi:[1,1,1]
	s_waitcnt vmcnt(9)
	v_cvt_scalef32_pk_f32_fp4 v[152:153], v20, 1.0
	v_cvt_scalef32_pk_f32_fp4 v[154:155], v20, 1.0 op_sel:[1,0,0]
	v_cvt_scalef32_pk_f32_fp4 v[156:157], v20, 1.0 op_sel:[0,1,0]
	v_cvt_scalef32_pk_f32_fp4 v[158:159], v20, 1.0 op_sel:[1,1,0]
	v_cvt_scalef32_pk_f32_fp4 v[160:161], v21, 1.0
	v_pk_fma_f32 v[120:121], v[226:227], v[152:153], v[120:121] op_sel_hi:[0,1,1]
	v_cvt_scalef32_pk_f32_fp4 v[162:163], v21, 1.0 op_sel:[1,0,0]
	v_pk_fma_f32 v[122:123], v[226:227], v[154:155], v[122:123] op_sel_hi:[0,1,1]
	v_cvt_scalef32_pk_f32_fp4 v[152:153], v21, 1.0 op_sel:[0,1,0]
	v_pk_fma_f32 v[124:125], v[226:227], v[156:157], v[124:125] op_sel_hi:[0,1,1]
	v_cvt_scalef32_pk_f32_fp4 v[154:155], v21, 1.0 op_sel:[1,1,0]
	v_pk_fma_f32 v[126:127], v[226:227], v[158:159], v[126:127] op_sel_hi:[0,1,1]
	v_cvt_scalef32_pk_f32_fp4 v[156:157], v22, 1.0
	v_pk_fma_f32 v[128:129], v[226:227], v[160:161], v[128:129] op_sel_hi:[0,1,1]
	v_cvt_scalef32_pk_f32_fp4 v[158:159], v22, 1.0 op_sel:[1,0,0]
	v_pk_fma_f32 v[130:131], v[226:227], v[162:163], v[130:131] op_sel_hi:[0,1,1]
	v_cvt_scalef32_pk_f32_fp4 v[160:161], v22, 1.0 op_sel:[0,1,0]
	v_pk_fma_f32 v[132:133], v[226:227], v[152:153], v[132:133] op_sel_hi:[0,1,1]
	v_cvt_scalef32_pk_f32_fp4 v[162:163], v22, 1.0 op_sel:[1,1,0]
	v_pk_fma_f32 v[134:135], v[226:227], v[154:155], v[134:135] op_sel_hi:[0,1,1]
	v_cvt_scalef32_pk_f32_fp4 v[152:153], v23, 1.0
	v_pk_fma_f32 v[136:137], v[226:227], v[156:157], v[136:137] op_sel_hi:[0,1,1]
	v_cvt_scalef32_pk_f32_fp4 v[154:155], v23, 1.0 op_sel:[1,0,0]
	v_pk_fma_f32 v[138:139], v[226:227], v[158:159], v[138:139] op_sel_hi:[0,1,1]
	v_cvt_scalef32_pk_f32_fp4 v[156:157], v23, 1.0 op_sel:[0,1,0]
	v_pk_fma_f32 v[140:141], v[226:227], v[160:161], v[140:141] op_sel_hi:[0,1,1]
	v_cvt_scalef32_pk_f32_fp4 v[158:159], v23, 1.0 op_sel:[1,1,0]
	v_pk_fma_f32 v[142:143], v[226:227], v[162:163], v[142:143] op_sel_hi:[0,1,1]
	v_pk_fma_f32 v[144:145], v[226:227], v[152:153], v[144:145] op_sel_hi:[0,1,1]
	v_pk_fma_f32 v[146:147], v[226:227], v[154:155], v[146:147] op_sel_hi:[0,1,1]
	v_pk_fma_f32 v[148:149], v[226:227], v[156:157], v[148:149] op_sel_hi:[0,1,1]
	v_pk_fma_f32 v[150:151], v[226:227], v[158:159], v[150:151] op_sel_hi:[0,1,1]
	s_waitcnt vmcnt(8)
	v_cvt_scalef32_pk_f32_fp4 v[152:153], v16, 1.0
	v_cvt_scalef32_pk_f32_fp4 v[154:155], v16, 1.0 op_sel:[1,0,0]
	v_cvt_scalef32_pk_f32_fp4 v[156:157], v16, 1.0 op_sel:[0,1,0]
	v_cvt_scalef32_pk_f32_fp4 v[158:159], v16, 1.0 op_sel:[1,1,0]
	v_cvt_scalef32_pk_f32_fp4 v[160:161], v17, 1.0
	v_pk_fma_f32 v[120:121], v[226:227], v[152:153], v[120:121] op_sel:[1,0,0] op_sel_hi:[1,1,1]
	v_cvt_scalef32_pk_f32_fp4 v[162:163], v17, 1.0 op_sel:[1,0,0]
	v_pk_fma_f32 v[122:123], v[226:227], v[154:155], v[122:123] op_sel:[1,0,0] op_sel_hi:[1,1,1]
	v_cvt_scalef32_pk_f32_fp4 v[152:153], v17, 1.0 op_sel:[0,1,0]
	v_pk_fma_f32 v[124:125], v[226:227], v[156:157], v[124:125] op_sel:[1,0,0] op_sel_hi:[1,1,1]
	v_cvt_scalef32_pk_f32_fp4 v[154:155], v17, 1.0 op_sel:[1,1,0]
	v_pk_fma_f32 v[126:127], v[226:227], v[158:159], v[126:127] op_sel:[1,0,0] op_sel_hi:[1,1,1]
	v_cvt_scalef32_pk_f32_fp4 v[156:157], v18, 1.0
	v_pk_fma_f32 v[128:129], v[226:227], v[160:161], v[128:129] op_sel:[1,0,0] op_sel_hi:[1,1,1]
	v_cvt_scalef32_pk_f32_fp4 v[158:159], v18, 1.0 op_sel:[1,0,0]
	v_pk_fma_f32 v[130:131], v[226:227], v[162:163], v[130:131] op_sel:[1,0,0] op_sel_hi:[1,1,1]
	v_cvt_scalef32_pk_f32_fp4 v[160:161], v18, 1.0 op_sel:[0,1,0]
	v_pk_fma_f32 v[132:133], v[226:227], v[152:153], v[132:133] op_sel:[1,0,0] op_sel_hi:[1,1,1]
	v_cvt_scalef32_pk_f32_fp4 v[162:163], v18, 1.0 op_sel:[1,1,0]
	v_pk_fma_f32 v[134:135], v[226:227], v[154:155], v[134:135] op_sel:[1,0,0] op_sel_hi:[1,1,1]
	v_cvt_scalef32_pk_f32_fp4 v[152:153], v19, 1.0
	v_pk_fma_f32 v[136:137], v[226:227], v[156:157], v[136:137] op_sel:[1,0,0] op_sel_hi:[1,1,1]
	v_cvt_scalef32_pk_f32_fp4 v[154:155], v19, 1.0 op_sel:[1,0,0]
	v_pk_fma_f32 v[138:139], v[226:227], v[158:159], v[138:139] op_sel:[1,0,0] op_sel_hi:[1,1,1]
	v_cvt_scalef32_pk_f32_fp4 v[156:157], v19, 1.0 op_sel:[0,1,0]
	v_pk_fma_f32 v[140:141], v[226:227], v[160:161], v[140:141] op_sel:[1,0,0] op_sel_hi:[1,1,1]
	v_cvt_scalef32_pk_f32_fp4 v[158:159], v19, 1.0 op_sel:[1,1,0]
	v_pk_fma_f32 v[142:143], v[226:227], v[162:163], v[142:143] op_sel:[1,0,0] op_sel_hi:[1,1,1]
	v_pk_fma_f32 v[144:145], v[226:227], v[152:153], v[144:145] op_sel:[1,0,0] op_sel_hi:[1,1,1]
	v_pk_fma_f32 v[146:147], v[226:227], v[154:155], v[146:147] op_sel:[1,0,0] op_sel_hi:[1,1,1]
	v_pk_fma_f32 v[148:149], v[226:227], v[156:157], v[148:149] op_sel:[1,0,0] op_sel_hi:[1,1,1]
	v_pk_fma_f32 v[150:151], v[226:227], v[158:159], v[150:151] op_sel:[1,0,0] op_sel_hi:[1,1,1]
	s_waitcnt vmcnt(7)
	v_cvt_scalef32_pk_f32_fp4 v[152:153], v12, 1.0
	v_cvt_scalef32_pk_f32_fp4 v[154:155], v12, 1.0 op_sel:[1,0,0]
	v_cvt_scalef32_pk_f32_fp4 v[156:157], v12, 1.0 op_sel:[0,1,0]
	v_cvt_scalef32_pk_f32_fp4 v[158:159], v12, 1.0 op_sel:[1,1,0]
	v_cvt_scalef32_pk_f32_fp4 v[160:161], v13, 1.0
	v_pk_fma_f32 v[120:121], v[228:229], v[152:153], v[120:121] op_sel_hi:[0,1,1]
	v_cvt_scalef32_pk_f32_fp4 v[162:163], v13, 1.0 op_sel:[1,0,0]
	v_pk_fma_f32 v[122:123], v[228:229], v[154:155], v[122:123] op_sel_hi:[0,1,1]
	v_cvt_scalef32_pk_f32_fp4 v[152:153], v13, 1.0 op_sel:[0,1,0]
	v_pk_fma_f32 v[124:125], v[228:229], v[156:157], v[124:125] op_sel_hi:[0,1,1]
	v_cvt_scalef32_pk_f32_fp4 v[154:155], v13, 1.0 op_sel:[1,1,0]
	v_pk_fma_f32 v[126:127], v[228:229], v[158:159], v[126:127] op_sel_hi:[0,1,1]
	v_cvt_scalef32_pk_f32_fp4 v[156:157], v14, 1.0
	v_pk_fma_f32 v[128:129], v[228:229], v[160:161], v[128:129] op_sel_hi:[0,1,1]
	v_cvt_scalef32_pk_f32_fp4 v[158:159], v14, 1.0 op_sel:[1,0,0]
	v_pk_fma_f32 v[130:131], v[228:229], v[162:163], v[130:131] op_sel_hi:[0,1,1]
	v_cvt_scalef32_pk_f32_fp4 v[160:161], v14, 1.0 op_sel:[0,1,0]
	v_pk_fma_f32 v[132:133], v[228:229], v[152:153], v[132:133] op_sel_hi:[0,1,1]
	v_cvt_scalef32_pk_f32_fp4 v[162:163], v14, 1.0 op_sel:[1,1,0]
	v_pk_fma_f32 v[134:135], v[228:229], v[154:155], v[134:135] op_sel_hi:[0,1,1]
	v_cvt_scalef32_pk_f32_fp4 v[152:153], v15, 1.0
	v_pk_fma_f32 v[136:137], v[228:229], v[156:157], v[136:137] op_sel_hi:[0,1,1]
	v_cvt_scalef32_pk_f32_fp4 v[154:155], v15, 1.0 op_sel:[1,0,0]
	v_pk_fma_f32 v[138:139], v[228:229], v[158:159], v[138:139] op_sel_hi:[0,1,1]
	v_cvt_scalef32_pk_f32_fp4 v[156:157], v15, 1.0 op_sel:[0,1,0]
	v_pk_fma_f32 v[140:141], v[228:229], v[160:161], v[140:141] op_sel_hi:[0,1,1]
	v_cvt_scalef32_pk_f32_fp4 v[158:159], v15, 1.0 op_sel:[1,1,0]
	v_pk_fma_f32 v[142:143], v[228:229], v[162:163], v[142:143] op_sel_hi:[0,1,1]
	v_pk_fma_f32 v[144:145], v[228:229], v[152:153], v[144:145] op_sel_hi:[0,1,1]
	v_pk_fma_f32 v[146:147], v[228:229], v[154:155], v[146:147] op_sel_hi:[0,1,1]
	v_pk_fma_f32 v[148:149], v[228:229], v[156:157], v[148:149] op_sel_hi:[0,1,1]
	v_pk_fma_f32 v[150:151], v[228:229], v[158:159], v[150:151] op_sel_hi:[0,1,1]
	s_waitcnt vmcnt(6)
	v_cvt_scalef32_pk_f32_fp4 v[152:153], v8, 1.0
	v_cvt_scalef32_pk_f32_fp4 v[154:155], v8, 1.0 op_sel:[1,0,0]
	v_cvt_scalef32_pk_f32_fp4 v[156:157], v8, 1.0 op_sel:[0,1,0]
	v_cvt_scalef32_pk_f32_fp4 v[158:159], v8, 1.0 op_sel:[1,1,0]
	v_cvt_scalef32_pk_f32_fp4 v[160:161], v9, 1.0
	v_pk_fma_f32 v[120:121], v[228:229], v[152:153], v[120:121] op_sel:[1,0,0] op_sel_hi:[1,1,1]
	v_cvt_scalef32_pk_f32_fp4 v[162:163], v9, 1.0 op_sel:[1,0,0]
	v_pk_fma_f32 v[122:123], v[228:229], v[154:155], v[122:123] op_sel:[1,0,0] op_sel_hi:[1,1,1]
	v_cvt_scalef32_pk_f32_fp4 v[152:153], v9, 1.0 op_sel:[0,1,0]
	v_pk_fma_f32 v[124:125], v[228:229], v[156:157], v[124:125] op_sel:[1,0,0] op_sel_hi:[1,1,1]
	v_cvt_scalef32_pk_f32_fp4 v[154:155], v9, 1.0 op_sel:[1,1,0]
	v_pk_fma_f32 v[126:127], v[228:229], v[158:159], v[126:127] op_sel:[1,0,0] op_sel_hi:[1,1,1]
	v_cvt_scalef32_pk_f32_fp4 v[156:157], v10, 1.0
	v_pk_fma_f32 v[128:129], v[228:229], v[160:161], v[128:129] op_sel:[1,0,0] op_sel_hi:[1,1,1]
	v_cvt_scalef32_pk_f32_fp4 v[158:159], v10, 1.0 op_sel:[1,0,0]
	v_pk_fma_f32 v[130:131], v[228:229], v[162:163], v[130:131] op_sel:[1,0,0] op_sel_hi:[1,1,1]
	v_cvt_scalef32_pk_f32_fp4 v[160:161], v10, 1.0 op_sel:[0,1,0]
	v_pk_fma_f32 v[132:133], v[228:229], v[152:153], v[132:133] op_sel:[1,0,0] op_sel_hi:[1,1,1]
	v_cvt_scalef32_pk_f32_fp4 v[162:163], v10, 1.0 op_sel:[1,1,0]
	v_pk_fma_f32 v[134:135], v[228:229], v[154:155], v[134:135] op_sel:[1,0,0] op_sel_hi:[1,1,1]
	v_cvt_scalef32_pk_f32_fp4 v[152:153], v11, 1.0
	v_pk_fma_f32 v[136:137], v[228:229], v[156:157], v[136:137] op_sel:[1,0,0] op_sel_hi:[1,1,1]
	v_cvt_scalef32_pk_f32_fp4 v[154:155], v11, 1.0 op_sel:[1,0,0]
	v_pk_fma_f32 v[138:139], v[228:229], v[158:159], v[138:139] op_sel:[1,0,0] op_sel_hi:[1,1,1]
	v_cvt_scalef32_pk_f32_fp4 v[156:157], v11, 1.0 op_sel:[0,1,0]
	v_pk_fma_f32 v[140:141], v[228:229], v[160:161], v[140:141] op_sel:[1,0,0] op_sel_hi:[1,1,1]
	v_cvt_scalef32_pk_f32_fp4 v[158:159], v11, 1.0 op_sel:[1,1,0]
	v_pk_fma_f32 v[142:143], v[228:229], v[162:163], v[142:143] op_sel:[1,0,0] op_sel_hi:[1,1,1]
	v_pk_fma_f32 v[144:145], v[228:229], v[152:153], v[144:145] op_sel:[1,0,0] op_sel_hi:[1,1,1]
	v_pk_fma_f32 v[146:147], v[228:229], v[154:155], v[146:147] op_sel:[1,0,0] op_sel_hi:[1,1,1]
	v_pk_fma_f32 v[148:149], v[228:229], v[156:157], v[148:149] op_sel:[1,0,0] op_sel_hi:[1,1,1]
	v_pk_fma_f32 v[150:151], v[228:229], v[158:159], v[150:151] op_sel:[1,0,0] op_sel_hi:[1,1,1]
	s_waitcnt vmcnt(5)
	v_cvt_scalef32_pk_f32_fp4 v[152:153], v4, 1.0
	v_cvt_scalef32_pk_f32_fp4 v[154:155], v4, 1.0 op_sel:[1,0,0]
	v_cvt_scalef32_pk_f32_fp4 v[156:157], v4, 1.0 op_sel:[0,1,0]
	v_cvt_scalef32_pk_f32_fp4 v[158:159], v4, 1.0 op_sel:[1,1,0]
	v_cvt_scalef32_pk_f32_fp4 v[160:161], v5, 1.0
	v_pk_fma_f32 v[120:121], v[230:231], v[152:153], v[120:121] op_sel_hi:[0,1,1]
	v_cvt_scalef32_pk_f32_fp4 v[162:163], v5, 1.0 op_sel:[1,0,0]
	v_pk_fma_f32 v[122:123], v[230:231], v[154:155], v[122:123] op_sel_hi:[0,1,1]
	v_cvt_scalef32_pk_f32_fp4 v[152:153], v5, 1.0 op_sel:[0,1,0]
	v_pk_fma_f32 v[124:125], v[230:231], v[156:157], v[124:125] op_sel_hi:[0,1,1]
	v_cvt_scalef32_pk_f32_fp4 v[154:155], v5, 1.0 op_sel:[1,1,0]
	v_pk_fma_f32 v[126:127], v[230:231], v[158:159], v[126:127] op_sel_hi:[0,1,1]
	v_cvt_scalef32_pk_f32_fp4 v[156:157], v6, 1.0
	v_pk_fma_f32 v[128:129], v[230:231], v[160:161], v[128:129] op_sel_hi:[0,1,1]
	v_cvt_scalef32_pk_f32_fp4 v[158:159], v6, 1.0 op_sel:[1,0,0]
	v_pk_fma_f32 v[130:131], v[230:231], v[162:163], v[130:131] op_sel_hi:[0,1,1]
	v_cvt_scalef32_pk_f32_fp4 v[160:161], v6, 1.0 op_sel:[0,1,0]
	v_pk_fma_f32 v[132:133], v[230:231], v[152:153], v[132:133] op_sel_hi:[0,1,1]
	v_cvt_scalef32_pk_f32_fp4 v[162:163], v6, 1.0 op_sel:[1,1,0]
	v_pk_fma_f32 v[134:135], v[230:231], v[154:155], v[134:135] op_sel_hi:[0,1,1]
	v_cvt_scalef32_pk_f32_fp4 v[152:153], v7, 1.0
	v_pk_fma_f32 v[136:137], v[230:231], v[156:157], v[136:137] op_sel_hi:[0,1,1]
	v_cvt_scalef32_pk_f32_fp4 v[154:155], v7, 1.0 op_sel:[1,0,0]
	v_pk_fma_f32 v[138:139], v[230:231], v[158:159], v[138:139] op_sel_hi:[0,1,1]
	v_cvt_scalef32_pk_f32_fp4 v[156:157], v7, 1.0 op_sel:[0,1,0]
	v_pk_fma_f32 v[140:141], v[230:231], v[160:161], v[140:141] op_sel_hi:[0,1,1]
	v_cvt_scalef32_pk_f32_fp4 v[158:159], v7, 1.0 op_sel:[1,1,0]
	v_pk_fma_f32 v[142:143], v[230:231], v[162:163], v[142:143] op_sel_hi:[0,1,1]
	v_pk_fma_f32 v[144:145], v[230:231], v[152:153], v[144:145] op_sel_hi:[0,1,1]
	v_pk_fma_f32 v[146:147], v[230:231], v[154:155], v[146:147] op_sel_hi:[0,1,1]
	v_pk_fma_f32 v[148:149], v[230:231], v[156:157], v[148:149] op_sel_hi:[0,1,1]
	v_pk_fma_f32 v[150:151], v[230:231], v[158:159], v[150:151] op_sel_hi:[0,1,1]
	s_waitcnt vmcnt(4)
	v_cvt_scalef32_pk_f32_fp4 v[152:153], v0, 1.0
	v_cvt_scalef32_pk_f32_fp4 v[154:155], v0, 1.0 op_sel:[1,0,0]
	v_cvt_scalef32_pk_f32_fp4 v[156:157], v0, 1.0 op_sel:[0,1,0]
	v_cvt_scalef32_pk_f32_fp4 v[158:159], v0, 1.0 op_sel:[1,1,0]
	v_cvt_scalef32_pk_f32_fp4 v[160:161], v1, 1.0
	v_pk_fma_f32 v[120:121], v[230:231], v[152:153], v[120:121] op_sel:[1,0,0] op_sel_hi:[1,1,1]
	v_cvt_scalef32_pk_f32_fp4 v[162:163], v1, 1.0 op_sel:[1,0,0]
	v_pk_fma_f32 v[122:123], v[230:231], v[154:155], v[122:123] op_sel:[1,0,0] op_sel_hi:[1,1,1]
	v_cvt_scalef32_pk_f32_fp4 v[152:153], v1, 1.0 op_sel:[0,1,0]
	v_pk_fma_f32 v[124:125], v[230:231], v[156:157], v[124:125] op_sel:[1,0,0] op_sel_hi:[1,1,1]
	v_cvt_scalef32_pk_f32_fp4 v[154:155], v1, 1.0 op_sel:[1,1,0]
	v_pk_fma_f32 v[126:127], v[230:231], v[158:159], v[126:127] op_sel:[1,0,0] op_sel_hi:[1,1,1]
	v_cvt_scalef32_pk_f32_fp4 v[156:157], v2, 1.0
	v_pk_fma_f32 v[128:129], v[230:231], v[160:161], v[128:129] op_sel:[1,0,0] op_sel_hi:[1,1,1]
	v_cvt_scalef32_pk_f32_fp4 v[158:159], v2, 1.0 op_sel:[1,0,0]
	v_pk_fma_f32 v[130:131], v[230:231], v[162:163], v[130:131] op_sel:[1,0,0] op_sel_hi:[1,1,1]
	v_cvt_scalef32_pk_f32_fp4 v[160:161], v2, 1.0 op_sel:[0,1,0]
	v_pk_fma_f32 v[132:133], v[230:231], v[152:153], v[132:133] op_sel:[1,0,0] op_sel_hi:[1,1,1]
	v_cvt_scalef32_pk_f32_fp4 v[162:163], v2, 1.0 op_sel:[1,1,0]
	v_pk_fma_f32 v[134:135], v[230:231], v[154:155], v[134:135] op_sel:[1,0,0] op_sel_hi:[1,1,1]
	v_cvt_scalef32_pk_f32_fp4 v[152:153], v3, 1.0
	v_pk_fma_f32 v[136:137], v[230:231], v[156:157], v[136:137] op_sel:[1,0,0] op_sel_hi:[1,1,1]
	v_cvt_scalef32_pk_f32_fp4 v[154:155], v3, 1.0 op_sel:[1,0,0]
	v_pk_fma_f32 v[138:139], v[230:231], v[158:159], v[138:139] op_sel:[1,0,0] op_sel_hi:[1,1,1]
	v_cvt_scalef32_pk_f32_fp4 v[156:157], v3, 1.0 op_sel:[0,1,0]
	v_pk_fma_f32 v[140:141], v[230:231], v[160:161], v[140:141] op_sel:[1,0,0] op_sel_hi:[1,1,1]
	v_cvt_scalef32_pk_f32_fp4 v[158:159], v3, 1.0 op_sel:[1,1,0]
	v_pk_fma_f32 v[142:143], v[230:231], v[162:163], v[142:143] op_sel:[1,0,0] op_sel_hi:[1,1,1]
	v_pk_fma_f32 v[144:145], v[230:231], v[152:153], v[144:145] op_sel:[1,0,0] op_sel_hi:[1,1,1]
	v_pk_fma_f32 v[146:147], v[230:231], v[154:155], v[146:147] op_sel:[1,0,0] op_sel_hi:[1,1,1]
	v_pk_fma_f32 v[148:149], v[230:231], v[156:157], v[148:149] op_sel:[1,0,0] op_sel_hi:[1,1,1]
	v_pk_fma_f32 v[150:151], v[230:231], v[158:159], v[150:151] op_sel:[1,0,0] op_sel_hi:[1,1,1]
	v_and_b32_e32 v170, 8, v44
	s_nop 0
	v_permlane32_swap_b32_e32 v120, v136
	v_permlane32_swap_b32_e32 v121, v137
	v_permlane32_swap_b32_e32 v122, v138
	v_permlane32_swap_b32_e32 v123, v139
	v_permlane32_swap_b32_e32 v124, v140
	v_permlane32_swap_b32_e32 v125, v141
	v_permlane32_swap_b32_e32 v126, v142
	v_permlane32_swap_b32_e32 v127, v143
	v_permlane32_swap_b32_e32 v128, v144
	v_permlane32_swap_b32_e32 v129, v145
	v_permlane32_swap_b32_e32 v130, v146
	v_permlane32_swap_b32_e32 v131, v147
	v_permlane32_swap_b32_e32 v132, v148
	v_permlane32_swap_b32_e32 v133, v149
	v_permlane32_swap_b32_e32 v134, v150
	v_permlane32_swap_b32_e32 v135, v151
	v_pk_add_f32 v[120:121], v[120:121], v[136:137]
	v_pk_add_f32 v[122:123], v[122:123], v[138:139]
	v_pk_add_f32 v[124:125], v[124:125], v[140:141]
	v_pk_add_f32 v[126:127], v[126:127], v[142:143]
	v_pk_add_f32 v[128:129], v[128:129], v[144:145]
	v_pk_add_f32 v[130:131], v[130:131], v[146:147]
	v_pk_add_f32 v[132:133], v[132:133], v[148:149]
	v_pk_add_f32 v[134:135], v[134:135], v[150:151]
	v_cmp_ne_u32_e32 vcc, 0, v170
	s_nop 0
	v_permlane16_swap_b32_e32 v120, v128
	v_permlane16_swap_b32_e32 v121, v129
	v_permlane16_swap_b32_e32 v122, v130
	v_permlane16_swap_b32_e32 v123, v131
	v_permlane16_swap_b32_e32 v124, v132
	v_permlane16_swap_b32_e32 v125, v133
	v_permlane16_swap_b32_e32 v126, v134
	v_permlane16_swap_b32_e32 v127, v135
	v_pk_add_f32 v[120:121], v[120:121], v[128:129]
	v_pk_add_f32 v[122:123], v[122:123], v[130:131]
	v_pk_add_f32 v[124:125], v[124:125], v[132:133]
	v_pk_add_f32 v[126:127], v[126:127], v[134:135]
	s_nop 1
	v_add_f32_dpp v136, v120, v120 row_ror:8 row_mask:0xf bank_mask:0xf
	v_add_f32_dpp v137, v121, v121 row_ror:8 row_mask:0xf bank_mask:0xf
	v_add_f32_dpp v138, v122, v122 row_ror:8 row_mask:0xf bank_mask:0xf
	v_add_f32_dpp v139, v123, v123 row_ror:8 row_mask:0xf bank_mask:0xf
	v_add_f32_dpp v140, v124, v124 row_ror:8 row_mask:0xf bank_mask:0xf
	v_add_f32_dpp v141, v125, v125 row_ror:8 row_mask:0xf bank_mask:0xf
	v_add_f32_dpp v142, v126, v126 row_ror:8 row_mask:0xf bank_mask:0xf
	v_add_f32_dpp v143, v127, v127 row_ror:8 row_mask:0xf bank_mask:0xf
	v_cndmask_b32_e32 v136, v136, v140, vcc
	v_cndmask_b32_e32 v137, v137, v141, vcc
	v_cndmask_b32_e32 v138, v138, v142, vcc
	v_cndmask_b32_e32 v139, v139, v143, vcc
	v_cvt_pk_bf16_f32 v0, v136, v137
	v_cvt_pk_bf16_f32 v1, v138, v139
	v_lshl_add_u64 v[2:3], v[52:53], 0, s[18:19]
	s_add_u32 s18, s18, 0x1000
	v_add_co_u32_e32 v2, vcc, s14, v2
	s_addc_u32 s19, s19, 0
	s_nop 0
	v_addc_co_u32_e32 v3, vcc, 0, v3, vcc
	s_cmp_eq_u32 s18, 0x10000
	global_store_dwordx2 v[2:3], v[0:1], off
	s_cbranch_scc0 .LBB0_1393
	s_branch .LBB0_1381
